# VALU trims: SwiGLU u+1 folded into up-bias and clamp bounds, cvt zero-inits dropped, MLA max tree as two max3 chains, bf16 GEMM first-touch MFMAs with C=0
# speedup vs baseline: 1.0051x; 1.0051x over previous
.LBB0_142:
	s_ashr_i32 s13, s12, 31
	s_lshl_b64 s[18:19], s[12:13], 11
	s_add_u32 s18, s29, s18
	s_addc_u32 s19, s30, s19
	s_and_b64 s[24:25], s[2:3], exec
	s_cselect_b32 s13, s19, s23
	s_cselect_b32 s47, s18, s22
	s_add_u32 s48, s20, 0x100
	s_addc_u32 s49, s21, 0
	s_add_u32 s20, s22, 0x40080
	s_addc_u32 s21, s23, 0
	s_mov_b32 s50, -2
	s_branch .LBB0_143
.Lmy_zba_0:
	v_mfma_f32_16x16x32_bf16 v[126:129], v[140:143], v[180:183], 0
	v_mfma_f32_16x16x32_bf16 v[122:125], v[148:151], v[180:183], 0
	v_mfma_f32_16x16x32_bf16 v[118:121], v[140:143], v[204:207], 0
	v_mfma_f32_16x16x32_bf16 v[110:113], v[148:151], v[204:207], 0
	v_mfma_f32_16x16x32_bf16 v[102:105], v[140:143], v[212:215], 0
	v_mfma_f32_16x16x32_bf16 v[94:97], v[148:151], v[212:215], 0
	v_mfma_f32_16x16x32_bf16 v[86:89], v[140:143], v[220:223], 0
	v_mfma_f32_16x16x32_bf16 v[78:81], v[148:151], v[220:223], 0
	v_mfma_f32_16x16x32_bf16 v[126:129], v[144:147], v[200:203], v[126:129]
	v_mfma_f32_16x16x32_bf16 v[122:125], v[152:155], v[200:203], v[122:125]
	v_mfma_f32_16x16x32_bf16 v[118:121], v[144:147], v[208:211], v[118:121]
	v_mfma_f32_16x16x32_bf16 v[110:113], v[152:155], v[208:211], v[110:113]
	v_mfma_f32_16x16x32_bf16 v[102:105], v[144:147], v[216:219], v[102:105]
	v_mfma_f32_16x16x32_bf16 v[94:97], v[152:155], v[216:219], v[94:97]
	v_mfma_f32_16x16x32_bf16 v[86:89], v[144:147], v[224:227], v[86:89]
	v_mfma_f32_16x16x32_bf16 v[78:81], v[152:155], v[224:227], v[78:81]
	s_setprio 0
	s_setprio 1
	v_mfma_f32_16x16x32_bf16 v[114:117], v[156:159], v[180:183], 0
	v_mfma_f32_16x16x32_bf16 v[106:109], v[172:175], v[180:183], 0
	v_mfma_f32_16x16x32_bf16 v[98:101], v[156:159], v[204:207], 0
	v_mfma_f32_16x16x32_bf16 v[90:93], v[172:175], v[204:207], 0
	v_mfma_f32_16x16x32_bf16 v[82:85], v[156:159], v[212:215], 0
	v_mfma_f32_16x16x32_bf16 v[74:77], v[172:175], v[212:215], 0
	v_mfma_f32_16x16x32_bf16 v[70:73], v[156:159], v[220:223], 0
	v_mfma_f32_16x16x32_bf16 v[66:69], v[172:175], v[220:223], 0
	v_mfma_f32_16x16x32_bf16 v[114:117], v[160:163], v[200:203], v[114:117]
	v_mfma_f32_16x16x32_bf16 v[106:109], v[176:179], v[200:203], v[106:109]
	v_mfma_f32_16x16x32_bf16 v[98:101], v[160:163], v[208:211], v[98:101]
	v_mfma_f32_16x16x32_bf16 v[90:93], v[176:179], v[208:211], v[90:93]
	v_mfma_f32_16x16x32_bf16 v[82:85], v[160:163], v[216:219], v[82:85]
	v_mfma_f32_16x16x32_bf16 v[74:77], v[176:179], v[216:219], v[74:77]
	v_mfma_f32_16x16x32_bf16 v[70:73], v[160:163], v[224:227], v[70:73]
	v_mfma_f32_16x16x32_bf16 v[66:69], v[176:179], v[224:227], v[66:69]
	s_branch .Lmy_zbja_0
.Lmy_zba_1:
	v_mfma_f32_16x16x32_bf16 v[62:65], v[140:143], v[180:183], 0
	v_mfma_f32_16x16x32_bf16 v[58:61], v[148:151], v[180:183], 0
	v_mfma_f32_16x16x32_bf16 v[54:57], v[140:143], v[204:207], 0
	v_mfma_f32_16x16x32_bf16 v[46:49], v[148:151], v[204:207], 0
	v_mfma_f32_16x16x32_bf16 v[38:41], v[140:143], v[212:215], 0
	v_mfma_f32_16x16x32_bf16 v[30:33], v[148:151], v[212:215], 0
	v_mfma_f32_16x16x32_bf16 v[22:25], v[140:143], v[220:223], 0
	v_mfma_f32_16x16x32_bf16 v[14:17], v[148:151], v[220:223], 0
	v_mfma_f32_16x16x32_bf16 v[62:65], v[144:147], v[200:203], v[62:65]
	v_mfma_f32_16x16x32_bf16 v[58:61], v[152:155], v[200:203], v[58:61]
	v_mfma_f32_16x16x32_bf16 v[54:57], v[144:147], v[208:211], v[54:57]
	v_mfma_f32_16x16x32_bf16 v[46:49], v[152:155], v[208:211], v[46:49]
	v_mfma_f32_16x16x32_bf16 v[38:41], v[144:147], v[216:219], v[38:41]
	v_mfma_f32_16x16x32_bf16 v[30:33], v[152:155], v[216:219], v[30:33]
	v_mfma_f32_16x16x32_bf16 v[22:25], v[144:147], v[224:227], v[22:25]
	v_mfma_f32_16x16x32_bf16 v[14:17], v[152:155], v[224:227], v[14:17]
	s_setprio 0
	s_setprio 1
	v_mfma_f32_16x16x32_bf16 v[50:53], v[156:159], v[180:183], 0
	v_mfma_f32_16x16x32_bf16 v[42:45], v[172:175], v[180:183], 0
	v_mfma_f32_16x16x32_bf16 v[34:37], v[156:159], v[204:207], 0
	v_mfma_f32_16x16x32_bf16 v[26:29], v[172:175], v[204:207], 0
	v_mfma_f32_16x16x32_bf16 v[18:21], v[156:159], v[212:215], 0
	v_mfma_f32_16x16x32_bf16 v[10:13], v[172:175], v[212:215], 0
	v_mfma_f32_16x16x32_bf16 v[6:9], v[156:159], v[220:223], 0
	v_mfma_f32_16x16x32_bf16 v[2:5], v[172:175], v[220:223], 0
	v_mfma_f32_16x16x32_bf16 v[50:53], v[160:163], v[200:203], v[50:53]
	v_mfma_f32_16x16x32_bf16 v[42:45], v[176:179], v[200:203], v[42:45]
	v_mfma_f32_16x16x32_bf16 v[34:37], v[160:163], v[208:211], v[34:37]
	v_mfma_f32_16x16x32_bf16 v[26:29], v[176:179], v[208:211], v[26:29]
	v_mfma_f32_16x16x32_bf16 v[18:21], v[160:163], v[216:219], v[18:21]
	v_mfma_f32_16x16x32_bf16 v[10:13], v[176:179], v[216:219], v[10:13]
	v_mfma_f32_16x16x32_bf16 v[6:9], v[160:163], v[224:227], v[6:9]
	v_mfma_f32_16x16x32_bf16 v[2:5], v[176:179], v[224:227], v[2:5]
	s_branch .Lmy_zbja_1
.LBB0_143:
	s_add_u32 s22, s20, 0xfffc0080
	s_addc_u32 s23, s21, -1
	s_add_i32 s51, 0, 0x10000
	s_cmp_eq_u32 s50, 12
	s_cselect_b32 s23, s13, s23
	s_cselect_b32 s22, s47, s22
	v_add_u32_e32 v139, s51, v136
	s_cselect_b32 s25, s15, s49
	s_cselect_b32 s24, s14, s48
	s_add_i32 s54, 0, 0x14000
	ds_read_b128 v[140:143], v139
	ds_read_b128 v[144:147], v139 offset:1024
	ds_read_b128 v[148:151], v139 offset:2048
	ds_read_b128 v[152:155], v139 offset:3072
	v_add_u32_e32 v139, s54, v136
	ds_read_b128 v[156:159], v139
	ds_read_b128 v[160:163], v139 offset:1024
	ds_read_b128 v[172:175], v139 offset:2048
	ds_read_b128 v[176:179], v139 offset:3072
	v_mov_b32_e32 v139, v1
	ds_read_b128 v[180:183], v138
	ds_read_b128 v[200:203], v138 offset:1024
	ds_read_b128 v[204:207], v138 offset:2048
	ds_read_b128 v[208:211], v138 offset:3072
	ds_read_b128 v[212:215], v138 offset:4096
	ds_read_b128 v[216:219], v138 offset:5120
	ds_read_b128 v[220:223], v138 offset:6144
	ds_read_b128 v[224:227], v138 offset:7168
	s_add_i32 m0, s17, 0xc000
	s_nop 0
	global_load_lds_dwordx4 v139, s[20:21]
	v_mov_b32_e32 v139, v133
	s_add_i32 m0, s17, 0xe000
	s_nop 0
	global_load_lds_dwordx4 v139, s[20:21]
	s_waitcnt vmcnt(8)
	s_waitcnt lgkmcnt(0)
	s_barrier
	s_setprio 1
	s_waitcnt lgkmcnt(0)
	s_cmp_eq_u32 s50, -2
	s_cbranch_scc1 .Lmy_zba_0
	v_mfma_f32_16x16x32_bf16 v[126:129], v[140:143], v[180:183], v[126:129]
	v_mfma_f32_16x16x32_bf16 v[122:125], v[148:151], v[180:183], v[122:125]
	v_mfma_f32_16x16x32_bf16 v[118:121], v[140:143], v[204:207], v[118:121]
	v_mfma_f32_16x16x32_bf16 v[110:113], v[148:151], v[204:207], v[110:113]
	v_mfma_f32_16x16x32_bf16 v[102:105], v[140:143], v[212:215], v[102:105]
	v_mfma_f32_16x16x32_bf16 v[94:97], v[148:151], v[212:215], v[94:97]
	v_mfma_f32_16x16x32_bf16 v[86:89], v[140:143], v[220:223], v[86:89]
	v_mfma_f32_16x16x32_bf16 v[78:81], v[148:151], v[220:223], v[78:81]
	v_mfma_f32_16x16x32_bf16 v[126:129], v[144:147], v[200:203], v[126:129]
	v_mfma_f32_16x16x32_bf16 v[122:125], v[152:155], v[200:203], v[122:125]
	v_mfma_f32_16x16x32_bf16 v[118:121], v[144:147], v[208:211], v[118:121]
	v_mfma_f32_16x16x32_bf16 v[110:113], v[152:155], v[208:211], v[110:113]
	v_mfma_f32_16x16x32_bf16 v[102:105], v[144:147], v[216:219], v[102:105]
	v_mfma_f32_16x16x32_bf16 v[94:97], v[152:155], v[216:219], v[94:97]
	v_mfma_f32_16x16x32_bf16 v[86:89], v[144:147], v[224:227], v[86:89]
	v_mfma_f32_16x16x32_bf16 v[78:81], v[152:155], v[224:227], v[78:81]
	s_setprio 0
	s_setprio 1
	v_mfma_f32_16x16x32_bf16 v[114:117], v[156:159], v[180:183], v[114:117]
	v_mfma_f32_16x16x32_bf16 v[106:109], v[172:175], v[180:183], v[106:109]
	v_mfma_f32_16x16x32_bf16 v[98:101], v[156:159], v[204:207], v[98:101]
	v_mfma_f32_16x16x32_bf16 v[90:93], v[172:175], v[204:207], v[90:93]
	v_mfma_f32_16x16x32_bf16 v[82:85], v[156:159], v[212:215], v[82:85]
	v_mfma_f32_16x16x32_bf16 v[74:77], v[172:175], v[212:215], v[74:77]
	v_mfma_f32_16x16x32_bf16 v[70:73], v[156:159], v[220:223], v[70:73]
	v_mfma_f32_16x16x32_bf16 v[66:69], v[172:175], v[220:223], v[66:69]
	v_mfma_f32_16x16x32_bf16 v[114:117], v[160:163], v[200:203], v[114:117]
	v_mfma_f32_16x16x32_bf16 v[106:109], v[176:179], v[200:203], v[106:109]
	v_mfma_f32_16x16x32_bf16 v[98:101], v[160:163], v[208:211], v[98:101]
	v_mfma_f32_16x16x32_bf16 v[90:93], v[176:179], v[208:211], v[90:93]
	v_mfma_f32_16x16x32_bf16 v[82:85], v[160:163], v[216:219], v[82:85]
	v_mfma_f32_16x16x32_bf16 v[74:77], v[176:179], v[216:219], v[74:77]
	v_mfma_f32_16x16x32_bf16 v[70:73], v[160:163], v[224:227], v[70:73]
	v_mfma_f32_16x16x32_bf16 v[66:69], v[176:179], v[224:227], v[66:69]
.Lmy_zbja_0:
	s_setprio 0
	s_barrier
	v_mov_b32_e32 v139, v132
	s_add_i32 s51, s51, s31
	ds_read_b128 v[180:183], v138 offset:16384
	ds_read_b128 v[200:203], v138 offset:17408
	ds_read_b128 v[204:207], v138 offset:18432
	ds_read_b128 v[208:211], v138 offset:19456
	ds_read_b128 v[212:215], v138 offset:20480
	ds_read_b128 v[216:219], v138 offset:21504
	ds_read_b128 v[220:223], v138 offset:22528
	ds_read_b128 v[224:227], v138 offset:23552
	s_mov_b32 m0, s51
	s_nop 0
	global_load_lds_dwordx4 v139, s[24:25]
	v_mov_b32_e32 v139, v134
	s_add_i32 m0, s51, 0x2000
	s_add_u32 s52, s24, 0x40000
	global_load_lds_dwordx4 v139, s[24:25]
	s_addc_u32 s53, s25, 0
	v_mov_b32_e32 v139, v132
	s_add_i32 s51, s54, s31
	s_mov_b32 m0, s51
	s_nop 0
	global_load_lds_dwordx4 v139, s[52:53]
	v_mov_b32_e32 v139, v134
	s_add_i32 m0, s51, 0x2000
	s_nop 0
	global_load_lds_dwordx4 v139, s[52:53]
	v_mov_b32_e32 v139, v1
	s_mov_b32 m0, s17
	s_nop 0
	global_load_lds_dwordx4 v139, s[22:23]
	v_mov_b32_e32 v139, v133
	s_mov_b32 m0, s37
	s_nop 0
	global_load_lds_dwordx4 v139, s[22:23]
	s_waitcnt vmcnt(8)
	s_waitcnt lgkmcnt(0)
	s_barrier
	s_setprio 1
	s_waitcnt lgkmcnt(0)
	s_cmp_eq_u32 s50, -2
	s_cbranch_scc1 .Lmy_zba_1
	v_mfma_f32_16x16x32_bf16 v[62:65], v[140:143], v[180:183], v[62:65]
	v_mfma_f32_16x16x32_bf16 v[58:61], v[148:151], v[180:183], v[58:61]
	v_mfma_f32_16x16x32_bf16 v[54:57], v[140:143], v[204:207], v[54:57]
	v_mfma_f32_16x16x32_bf16 v[46:49], v[148:151], v[204:207], v[46:49]
	v_mfma_f32_16x16x32_bf16 v[38:41], v[140:143], v[212:215], v[38:41]
	v_mfma_f32_16x16x32_bf16 v[30:33], v[148:151], v[212:215], v[30:33]
	v_mfma_f32_16x16x32_bf16 v[22:25], v[140:143], v[220:223], v[22:25]
	v_mfma_f32_16x16x32_bf16 v[14:17], v[148:151], v[220:223], v[14:17]
	v_mfma_f32_16x16x32_bf16 v[62:65], v[144:147], v[200:203], v[62:65]
	v_mfma_f32_16x16x32_bf16 v[58:61], v[152:155], v[200:203], v[58:61]
	v_mfma_f32_16x16x32_bf16 v[54:57], v[144:147], v[208:211], v[54:57]
	v_mfma_f32_16x16x32_bf16 v[46:49], v[152:155], v[208:211], v[46:49]
	v_mfma_f32_16x16x32_bf16 v[38:41], v[144:147], v[216:219], v[38:41]
	v_mfma_f32_16x16x32_bf16 v[30:33], v[152:155], v[216:219], v[30:33]
	v_mfma_f32_16x16x32_bf16 v[22:25], v[144:147], v[224:227], v[22:25]
	v_mfma_f32_16x16x32_bf16 v[14:17], v[152:155], v[224:227], v[14:17]
	s_setprio 0
	s_setprio 1
	v_mfma_f32_16x16x32_bf16 v[50:53], v[156:159], v[180:183], v[50:53]
	v_mfma_f32_16x16x32_bf16 v[42:45], v[172:175], v[180:183], v[42:45]
	v_mfma_f32_16x16x32_bf16 v[34:37], v[156:159], v[204:207], v[34:37]
	v_mfma_f32_16x16x32_bf16 v[26:29], v[172:175], v[204:207], v[26:29]
	v_mfma_f32_16x16x32_bf16 v[18:21], v[156:159], v[212:215], v[18:21]
	v_mfma_f32_16x16x32_bf16 v[10:13], v[172:175], v[212:215], v[10:13]
	v_mfma_f32_16x16x32_bf16 v[6:9], v[156:159], v[220:223], v[6:9]
	v_mfma_f32_16x16x32_bf16 v[2:5], v[172:175], v[220:223], v[2:5]
	v_mfma_f32_16x16x32_bf16 v[50:53], v[160:163], v[200:203], v[50:53]
	v_mfma_f32_16x16x32_bf16 v[42:45], v[176:179], v[200:203], v[42:45]
	v_mfma_f32_16x16x32_bf16 v[34:37], v[160:163], v[208:211], v[34:37]
	v_mfma_f32_16x16x32_bf16 v[26:29], v[176:179], v[208:211], v[26:29]
	v_mfma_f32_16x16x32_bf16 v[18:21], v[160:163], v[216:219], v[18:21]
	v_mfma_f32_16x16x32_bf16 v[10:13], v[176:179], v[216:219], v[10:13]
	v_mfma_f32_16x16x32_bf16 v[6:9], v[160:163], v[224:227], v[6:9]
	v_mfma_f32_16x16x32_bf16 v[2:5], v[176:179], v[224:227], v[2:5]
.Lmy_zbja_1:
	s_setprio 0
	s_barrier
	s_add_i32 s51, 0, 0x18000
	v_add_u32_e32 v139, s51, v136
	s_add_i32 s54, 0, 0x1c000
	ds_read_b128 v[140:143], v139
	ds_read_b128 v[144:147], v139 offset:1024
	ds_read_b128 v[148:151], v139 offset:2048
	ds_read_b128 v[152:155], v139 offset:3072
	v_add_u32_e32 v139, s54, v136
	ds_read_b128 v[156:159], v139
	ds_read_b128 v[160:163], v139 offset:1024
	ds_read_b128 v[172:175], v139 offset:2048
	ds_read_b128 v[176:179], v139 offset:3072
	s_add_u32 s52, s22, 0x40000
	v_mov_b32_e32 v139, v1
	s_mov_b32 m0, s40
	ds_read_b128 v[180:183], v138 offset:32768
	ds_read_b128 v[200:203], v138 offset:33792
	ds_read_b128 v[204:207], v138 offset:34816
	ds_read_b128 v[208:211], v138 offset:35840
	ds_read_b128 v[212:215], v138 offset:36864
	ds_read_b128 v[216:219], v138 offset:37888
	ds_read_b128 v[220:223], v138 offset:38912
	ds_read_b128 v[224:227], v138 offset:39936
	s_addc_u32 s53, s23, 0
	s_nop 0
	global_load_lds_dwordx4 v139, s[52:53]
	v_mov_b32_e32 v139, v133
	s_mov_b32 m0, s41
	s_nop 0
	global_load_lds_dwordx4 v139, s[52:53]
	s_waitcnt vmcnt(8)
	s_waitcnt lgkmcnt(0)
	s_barrier
	s_setprio 1
	s_waitcnt lgkmcnt(0)
	v_mfma_f32_16x16x32_bf16 v[126:129], v[140:143], v[180:183], v[126:129]
	v_mfma_f32_16x16x32_bf16 v[122:125], v[148:151], v[180:183], v[122:125]
	v_mfma_f32_16x16x32_bf16 v[118:121], v[140:143], v[204:207], v[118:121]
	v_mfma_f32_16x16x32_bf16 v[110:113], v[148:151], v[204:207], v[110:113]
	v_mfma_f32_16x16x32_bf16 v[102:105], v[140:143], v[212:215], v[102:105]
	v_mfma_f32_16x16x32_bf16 v[94:97], v[148:151], v[212:215], v[94:97]
	v_mfma_f32_16x16x32_bf16 v[86:89], v[140:143], v[220:223], v[86:89]
	v_mfma_f32_16x16x32_bf16 v[78:81], v[148:151], v[220:223], v[78:81]
	v_mfma_f32_16x16x32_bf16 v[126:129], v[144:147], v[200:203], v[126:129]
	v_mfma_f32_16x16x32_bf16 v[122:125], v[152:155], v[200:203], v[122:125]
	v_mfma_f32_16x16x32_bf16 v[118:121], v[144:147], v[208:211], v[118:121]
	v_mfma_f32_16x16x32_bf16 v[110:113], v[152:155], v[208:211], v[110:113]
	v_mfma_f32_16x16x32_bf16 v[102:105], v[144:147], v[216:219], v[102:105]
	v_mfma_f32_16x16x32_bf16 v[94:97], v[152:155], v[216:219], v[94:97]
	v_mfma_f32_16x16x32_bf16 v[86:89], v[144:147], v[224:227], v[86:89]
	v_mfma_f32_16x16x32_bf16 v[78:81], v[152:155], v[224:227], v[78:81]
	s_setprio 0
	s_setprio 1
	v_mfma_f32_16x16x32_bf16 v[114:117], v[156:159], v[180:183], v[114:117]
	v_mfma_f32_16x16x32_bf16 v[106:109], v[172:175], v[180:183], v[106:109]
	v_mfma_f32_16x16x32_bf16 v[98:101], v[156:159], v[204:207], v[98:101]
	v_mfma_f32_16x16x32_bf16 v[90:93], v[172:175], v[204:207], v[90:93]
	v_mfma_f32_16x16x32_bf16 v[82:85], v[156:159], v[212:215], v[82:85]
	v_mfma_f32_16x16x32_bf16 v[74:77], v[172:175], v[212:215], v[74:77]
	v_mfma_f32_16x16x32_bf16 v[70:73], v[156:159], v[220:223], v[70:73]
	v_mfma_f32_16x16x32_bf16 v[66:69], v[172:175], v[220:223], v[66:69]
	v_mfma_f32_16x16x32_bf16 v[114:117], v[160:163], v[200:203], v[114:117]
	v_mfma_f32_16x16x32_bf16 v[106:109], v[176:179], v[200:203], v[106:109]
	v_mfma_f32_16x16x32_bf16 v[98:101], v[160:163], v[208:211], v[98:101]
	v_mfma_f32_16x16x32_bf16 v[90:93], v[176:179], v[208:211], v[90:93]
	v_mfma_f32_16x16x32_bf16 v[82:85], v[160:163], v[216:219], v[82:85]
	v_mfma_f32_16x16x32_bf16 v[74:77], v[176:179], v[216:219], v[74:77]
	v_mfma_f32_16x16x32_bf16 v[70:73], v[160:163], v[224:227], v[70:73]
	v_mfma_f32_16x16x32_bf16 v[66:69], v[176:179], v[224:227], v[66:69]
	s_setprio 0
	s_barrier
	v_mov_b32_e32 v166, v132
	ds_read_b128 v[180:183], v138 offset:49152
	ds_read_b128 v[200:203], v138 offset:50176
	ds_read_b128 v[204:207], v138 offset:51200
	ds_read_b128 v[208:211], v138 offset:52224
	ds_read_b128 v[212:215], v138 offset:53248
	ds_read_b128 v[216:219], v138 offset:54272
	ds_read_b128 v[220:223], v138 offset:55296
	ds_read_b128 v[224:227], v138 offset:56320
	s_add_i32 s51, s51, s31
	v_lshl_add_u64 v[164:165], s[24:25], 0, v[166:167]
	v_lshl_add_u64 v[164:165], v[164:165], 0, s[80:81]
	s_mov_b32 m0, s51
	v_mov_b32_e32 v166, v134
	global_load_lds_dwordx4 v[164:165], off
	s_add_i32 m0, s51, 0x2000
	v_mov_b32_e32 v139, v132
	v_lshl_add_u64 v[164:165], s[24:25], 0, v[166:167]
	s_add_u32 s24, s24, 0x40080
	v_lshl_add_u64 v[164:165], v[164:165], 0, s[80:81]
	s_addc_u32 s25, s25, 0
	s_add_i32 s51, s54, s31
	global_load_lds_dwordx4 v[164:165], off
	s_mov_b32 m0, s51
	v_mov_b32_e32 v166, v1
	global_load_lds_dwordx4 v139, s[24:25]
	v_mov_b32_e32 v139, v134
	s_add_i32 m0, s51, 0x2000
	s_nop 0
	global_load_lds_dwordx4 v139, s[24:25]
	s_mov_b32 m0, s42
	v_lshl_add_u64 v[164:165], s[22:23], 0, v[166:167]
	v_lshl_add_u64 v[164:165], v[164:165], 0, s[80:81]
	v_mov_b32_e32 v166, v133
	global_load_lds_dwordx4 v[164:165], off
	s_mov_b32 m0, s43
	v_lshl_add_u64 v[164:165], s[22:23], 0, v[166:167]
	v_lshl_add_u64 v[164:165], v[164:165], 0, s[80:81]
	global_load_lds_dwordx4 v[164:165], off
	s_waitcnt vmcnt(8)
	s_waitcnt lgkmcnt(0)
	s_barrier
	s_setprio 1
	s_waitcnt lgkmcnt(0)
	v_mfma_f32_16x16x32_bf16 v[62:65], v[140:143], v[180:183], v[62:65]
	v_mfma_f32_16x16x32_bf16 v[58:61], v[148:151], v[180:183], v[58:61]
	v_mfma_f32_16x16x32_bf16 v[54:57], v[140:143], v[204:207], v[54:57]
	v_mfma_f32_16x16x32_bf16 v[46:49], v[148:151], v[204:207], v[46:49]
	v_mfma_f32_16x16x32_bf16 v[38:41], v[140:143], v[212:215], v[38:41]
	v_mfma_f32_16x16x32_bf16 v[30:33], v[148:151], v[212:215], v[30:33]
	v_mfma_f32_16x16x32_bf16 v[22:25], v[140:143], v[220:223], v[22:25]
	v_mfma_f32_16x16x32_bf16 v[14:17], v[148:151], v[220:223], v[14:17]
	v_mfma_f32_16x16x32_bf16 v[62:65], v[144:147], v[200:203], v[62:65]
	v_mfma_f32_16x16x32_bf16 v[58:61], v[152:155], v[200:203], v[58:61]
	v_mfma_f32_16x16x32_bf16 v[54:57], v[144:147], v[208:211], v[54:57]
	v_mfma_f32_16x16x32_bf16 v[46:49], v[152:155], v[208:211], v[46:49]
	v_mfma_f32_16x16x32_bf16 v[38:41], v[144:147], v[216:219], v[38:41]
	v_mfma_f32_16x16x32_bf16 v[30:33], v[152:155], v[216:219], v[30:33]
	v_mfma_f32_16x16x32_bf16 v[22:25], v[144:147], v[224:227], v[22:25]
	v_mfma_f32_16x16x32_bf16 v[14:17], v[152:155], v[224:227], v[14:17]
	s_setprio 0
	s_setprio 1
	v_mfma_f32_16x16x32_bf16 v[50:53], v[156:159], v[180:183], v[50:53]
	v_mfma_f32_16x16x32_bf16 v[42:45], v[172:175], v[180:183], v[42:45]
	v_mfma_f32_16x16x32_bf16 v[34:37], v[156:159], v[204:207], v[34:37]
	v_mfma_f32_16x16x32_bf16 v[26:29], v[172:175], v[204:207], v[26:29]
	v_mfma_f32_16x16x32_bf16 v[18:21], v[156:159], v[212:215], v[18:21]
	v_mfma_f32_16x16x32_bf16 v[10:13], v[172:175], v[212:215], v[10:13]
	v_mfma_f32_16x16x32_bf16 v[6:9], v[156:159], v[220:223], v[6:9]
	v_mfma_f32_16x16x32_bf16 v[2:5], v[172:175], v[220:223], v[2:5]
	v_mfma_f32_16x16x32_bf16 v[50:53], v[160:163], v[200:203], v[50:53]
	v_mfma_f32_16x16x32_bf16 v[42:45], v[176:179], v[200:203], v[42:45]
	v_mfma_f32_16x16x32_bf16 v[34:37], v[160:163], v[208:211], v[34:37]
	v_mfma_f32_16x16x32_bf16 v[26:29], v[176:179], v[208:211], v[26:29]
	v_mfma_f32_16x16x32_bf16 v[18:21], v[160:163], v[216:219], v[18:21]
	v_mfma_f32_16x16x32_bf16 v[10:13], v[176:179], v[216:219], v[10:13]
	v_mfma_f32_16x16x32_bf16 v[6:9], v[160:163], v[224:227], v[6:9]
	v_mfma_f32_16x16x32_bf16 v[2:5], v[176:179], v[224:227], v[2:5]
	s_setprio 0
	s_barrier
	s_add_i32 s50, s50, 2
	s_add_u32 s48, s48, 0x100
	s_addc_u32 s49, s49, 0
	s_add_u32 s20, s20, 0x100
	s_addc_u32 s21, s21, 0
	s_cmp_gt_u32 s50, 13
	s_cbranch_scc0 .LBB0_143
	s_and_b64 vcc, exec, s[10:11]
	s_cbranch_vccz .LBB0_146
	s_barrier

.LBB0_167:
	s_ashr_i32 s11, s10, 31
	s_lshl_b64 s[14:15], s[10:11], 11
	s_add_u32 s14, s24, s14
	s_addc_u32 s15, s25, s15
	s_and_b64 s[20:21], s[2:3], exec
	s_cselect_b32 s11, s15, s19
	s_cselect_b32 s41, s14, s18
	s_add_u32 s42, s16, 0x100
	s_addc_u32 s43, s17, 0
	s_add_u32 s16, s18, 0x40080
	s_addc_u32 s17, s19, 0
	s_mov_b32 s44, -2
	s_branch .LBB0_168
.Lmy_zbb_0:
	v_mfma_f32_16x16x32_bf16 v[126:129], v[138:141], v[176:179], 0
	v_mfma_f32_16x16x32_bf16 v[122:125], v[146:149], v[176:179], 0
	v_mfma_f32_16x16x32_bf16 v[118:121], v[138:141], v[200:203], 0
	v_mfma_f32_16x16x32_bf16 v[114:117], v[146:149], v[200:203], 0
	v_mfma_f32_16x16x32_bf16 v[102:105], v[138:141], v[208:211], 0
	v_mfma_f32_16x16x32_bf16 v[98:101], v[146:149], v[208:211], 0
	v_mfma_f32_16x16x32_bf16 v[86:89], v[138:141], v[216:219], 0
	v_mfma_f32_16x16x32_bf16 v[82:85], v[146:149], v[216:219], 0
	v_mfma_f32_16x16x32_bf16 v[126:129], v[142:145], v[180:183], v[126:129]
	v_mfma_f32_16x16x32_bf16 v[122:125], v[150:153], v[180:183], v[122:125]
	v_mfma_f32_16x16x32_bf16 v[118:121], v[142:145], v[204:207], v[118:121]
	v_mfma_f32_16x16x32_bf16 v[114:117], v[150:153], v[204:207], v[114:117]
	v_mfma_f32_16x16x32_bf16 v[102:105], v[142:145], v[212:215], v[102:105]
	v_mfma_f32_16x16x32_bf16 v[98:101], v[150:153], v[212:215], v[98:101]
	v_mfma_f32_16x16x32_bf16 v[86:89], v[142:145], v[220:223], v[86:89]
	v_mfma_f32_16x16x32_bf16 v[82:85], v[150:153], v[220:223], v[82:85]
	s_setprio 0
	s_setprio 1
	v_mfma_f32_16x16x32_bf16 v[110:113], v[154:157], v[176:179], 0
	v_mfma_f32_16x16x32_bf16 v[106:109], v[162:165], v[176:179], 0
	v_mfma_f32_16x16x32_bf16 v[94:97], v[154:157], v[200:203], 0
	v_mfma_f32_16x16x32_bf16 v[90:93], v[162:165], v[200:203], 0
	v_mfma_f32_16x16x32_bf16 v[78:81], v[154:157], v[208:211], 0
	v_mfma_f32_16x16x32_bf16 v[74:77], v[162:165], v[208:211], 0
	v_mfma_f32_16x16x32_bf16 v[70:73], v[154:157], v[216:219], 0
	v_mfma_f32_16x16x32_bf16 v[62:65], v[162:165], v[216:219], 0
	v_mfma_f32_16x16x32_bf16 v[110:113], v[158:161], v[180:183], v[110:113]
	v_mfma_f32_16x16x32_bf16 v[106:109], v[172:175], v[180:183], v[106:109]
	v_mfma_f32_16x16x32_bf16 v[94:97], v[158:161], v[204:207], v[94:97]
	v_mfma_f32_16x16x32_bf16 v[90:93], v[172:175], v[204:207], v[90:93]
	v_mfma_f32_16x16x32_bf16 v[78:81], v[158:161], v[212:215], v[78:81]
	v_mfma_f32_16x16x32_bf16 v[74:77], v[172:175], v[212:215], v[74:77]
	v_mfma_f32_16x16x32_bf16 v[70:73], v[158:161], v[220:223], v[70:73]
	v_mfma_f32_16x16x32_bf16 v[62:65], v[172:175], v[220:223], v[62:65]
	s_branch .Lmy_zbjb_0
.Lmy_zbb_1:
	v_mfma_f32_16x16x32_bf16 v[66:69], v[138:141], v[176:179], 0
	v_mfma_f32_16x16x32_bf16 v[58:61], v[146:149], v[176:179], 0
	v_mfma_f32_16x16x32_bf16 v[54:57], v[138:141], v[200:203], 0
	v_mfma_f32_16x16x32_bf16 v[50:53], v[146:149], v[200:203], 0
	v_mfma_f32_16x16x32_bf16 v[38:41], v[138:141], v[208:211], 0
	v_mfma_f32_16x16x32_bf16 v[34:37], v[146:149], v[208:211], 0
	v_mfma_f32_16x16x32_bf16 v[22:25], v[138:141], v[216:219], 0
	v_mfma_f32_16x16x32_bf16 v[18:21], v[146:149], v[216:219], 0
	v_mfma_f32_16x16x32_bf16 v[66:69], v[142:145], v[180:183], v[66:69]
	v_mfma_f32_16x16x32_bf16 v[58:61], v[150:153], v[180:183], v[58:61]
	v_mfma_f32_16x16x32_bf16 v[54:57], v[142:145], v[204:207], v[54:57]
	v_mfma_f32_16x16x32_bf16 v[50:53], v[150:153], v[204:207], v[50:53]
	v_mfma_f32_16x16x32_bf16 v[38:41], v[142:145], v[212:215], v[38:41]
	v_mfma_f32_16x16x32_bf16 v[34:37], v[150:153], v[212:215], v[34:37]
	v_mfma_f32_16x16x32_bf16 v[22:25], v[142:145], v[220:223], v[22:25]
	v_mfma_f32_16x16x32_bf16 v[18:21], v[150:153], v[220:223], v[18:21]
	s_setprio 0
	s_setprio 1
	v_mfma_f32_16x16x32_bf16 v[46:49], v[154:157], v[176:179], 0
	v_mfma_f32_16x16x32_bf16 v[42:45], v[162:165], v[176:179], 0
	v_mfma_f32_16x16x32_bf16 v[30:33], v[154:157], v[200:203], 0
	v_mfma_f32_16x16x32_bf16 v[26:29], v[162:165], v[200:203], 0
	v_mfma_f32_16x16x32_bf16 v[14:17], v[154:157], v[208:211], 0
	v_mfma_f32_16x16x32_bf16 v[10:13], v[162:165], v[208:211], 0
	v_mfma_f32_16x16x32_bf16 v[6:9], v[154:157], v[216:219], 0
	v_mfma_f32_16x16x32_bf16 v[2:5], v[162:165], v[216:219], 0
	v_mfma_f32_16x16x32_bf16 v[46:49], v[158:161], v[180:183], v[46:49]
	v_mfma_f32_16x16x32_bf16 v[42:45], v[172:175], v[180:183], v[42:45]
	v_mfma_f32_16x16x32_bf16 v[30:33], v[158:161], v[204:207], v[30:33]
	v_mfma_f32_16x16x32_bf16 v[26:29], v[172:175], v[204:207], v[26:29]
	v_mfma_f32_16x16x32_bf16 v[14:17], v[158:161], v[212:215], v[14:17]
	v_mfma_f32_16x16x32_bf16 v[10:13], v[172:175], v[212:215], v[10:13]
	v_mfma_f32_16x16x32_bf16 v[6:9], v[158:161], v[220:223], v[6:9]
	v_mfma_f32_16x16x32_bf16 v[2:5], v[172:175], v[220:223], v[2:5]
	s_branch .Lmy_zbjb_1
.LBB0_168:
	s_add_u32 s18, s16, 0xfffc0080
	s_addc_u32 s19, s17, -1
	s_add_i32 s45, 0, 0x10000
	s_cmp_eq_u32 s44, 12
	s_cselect_b32 s19, s11, s19
	s_cselect_b32 s18, s41, s18
	v_add_u32_e32 v137, s45, v134
	s_cselect_b32 s21, s13, s43
	s_cselect_b32 s20, s12, s42
	s_add_i32 s48, 0, 0x14000
	ds_read_b128 v[138:141], v137
	ds_read_b128 v[142:145], v137 offset:1024
	ds_read_b128 v[146:149], v137 offset:2048
	ds_read_b128 v[150:153], v137 offset:3072
	v_add_u32_e32 v137, s48, v134
	ds_read_b128 v[154:157], v137
	ds_read_b128 v[158:161], v137 offset:1024
	ds_read_b128 v[162:165], v137 offset:2048
	ds_read_b128 v[172:175], v137 offset:3072
	v_mov_b32_e32 v137, v1
	ds_read_b128 v[176:179], v136
	ds_read_b128 v[180:183], v136 offset:1024
	ds_read_b128 v[200:203], v136 offset:2048
	ds_read_b128 v[204:207], v136 offset:3072
	ds_read_b128 v[208:211], v136 offset:4096
	ds_read_b128 v[212:215], v136 offset:5120
	ds_read_b128 v[216:219], v136 offset:6144
	ds_read_b128 v[220:223], v136 offset:7168
	s_add_i32 m0, s7, 0xc000
	s_nop 0
	global_load_lds_dwordx4 v137, s[16:17]
	v_mov_b32_e32 v137, v131
	s_add_i32 m0, s7, 0xe000
	s_nop 0
	global_load_lds_dwordx4 v137, s[16:17]
	s_waitcnt vmcnt(8)
	s_waitcnt lgkmcnt(0)
	s_barrier
	s_setprio 1
	s_waitcnt lgkmcnt(0)
	s_cmp_eq_u32 s44, -2
	s_cbranch_scc1 .Lmy_zbb_0
	v_mfma_f32_16x16x32_bf16 v[126:129], v[138:141], v[176:179], v[126:129]
	v_mfma_f32_16x16x32_bf16 v[122:125], v[146:149], v[176:179], v[122:125]
	v_mfma_f32_16x16x32_bf16 v[118:121], v[138:141], v[200:203], v[118:121]
	v_mfma_f32_16x16x32_bf16 v[114:117], v[146:149], v[200:203], v[114:117]
	v_mfma_f32_16x16x32_bf16 v[102:105], v[138:141], v[208:211], v[102:105]
	v_mfma_f32_16x16x32_bf16 v[98:101], v[146:149], v[208:211], v[98:101]
	v_mfma_f32_16x16x32_bf16 v[86:89], v[138:141], v[216:219], v[86:89]
	v_mfma_f32_16x16x32_bf16 v[82:85], v[146:149], v[216:219], v[82:85]
	v_mfma_f32_16x16x32_bf16 v[126:129], v[142:145], v[180:183], v[126:129]
	v_mfma_f32_16x16x32_bf16 v[122:125], v[150:153], v[180:183], v[122:125]
	v_mfma_f32_16x16x32_bf16 v[118:121], v[142:145], v[204:207], v[118:121]
	v_mfma_f32_16x16x32_bf16 v[114:117], v[150:153], v[204:207], v[114:117]
	v_mfma_f32_16x16x32_bf16 v[102:105], v[142:145], v[212:215], v[102:105]
	v_mfma_f32_16x16x32_bf16 v[98:101], v[150:153], v[212:215], v[98:101]
	v_mfma_f32_16x16x32_bf16 v[86:89], v[142:145], v[220:223], v[86:89]
	v_mfma_f32_16x16x32_bf16 v[82:85], v[150:153], v[220:223], v[82:85]
	s_setprio 0
	s_setprio 1
	v_mfma_f32_16x16x32_bf16 v[110:113], v[154:157], v[176:179], v[110:113]
	v_mfma_f32_16x16x32_bf16 v[106:109], v[162:165], v[176:179], v[106:109]
	v_mfma_f32_16x16x32_bf16 v[94:97], v[154:157], v[200:203], v[94:97]
	v_mfma_f32_16x16x32_bf16 v[90:93], v[162:165], v[200:203], v[90:93]
	v_mfma_f32_16x16x32_bf16 v[78:81], v[154:157], v[208:211], v[78:81]
	v_mfma_f32_16x16x32_bf16 v[74:77], v[162:165], v[208:211], v[74:77]
	v_mfma_f32_16x16x32_bf16 v[70:73], v[154:157], v[216:219], v[70:73]
	v_mfma_f32_16x16x32_bf16 v[62:65], v[162:165], v[216:219], v[62:65]
	v_mfma_f32_16x16x32_bf16 v[110:113], v[158:161], v[180:183], v[110:113]
	v_mfma_f32_16x16x32_bf16 v[106:109], v[172:175], v[180:183], v[106:109]
	v_mfma_f32_16x16x32_bf16 v[94:97], v[158:161], v[204:207], v[94:97]
	v_mfma_f32_16x16x32_bf16 v[90:93], v[172:175], v[204:207], v[90:93]
	v_mfma_f32_16x16x32_bf16 v[78:81], v[158:161], v[212:215], v[78:81]
	v_mfma_f32_16x16x32_bf16 v[74:77], v[172:175], v[212:215], v[74:77]
	v_mfma_f32_16x16x32_bf16 v[70:73], v[158:161], v[220:223], v[70:73]
	v_mfma_f32_16x16x32_bf16 v[62:65], v[172:175], v[220:223], v[62:65]
.Lmy_zbjb_0:
	s_setprio 0
	s_barrier
	v_mov_b32_e32 v137, v130
	s_add_i32 s45, s45, s28
	ds_read_b128 v[176:179], v136 offset:16384
	ds_read_b128 v[180:183], v136 offset:17408
	ds_read_b128 v[200:203], v136 offset:18432
	ds_read_b128 v[204:207], v136 offset:19456
	ds_read_b128 v[208:211], v136 offset:20480
	ds_read_b128 v[212:215], v136 offset:21504
	ds_read_b128 v[216:219], v136 offset:22528
	ds_read_b128 v[220:223], v136 offset:23552
	s_mov_b32 m0, s45
	s_nop 0
	global_load_lds_dwordx4 v137, s[20:21]
	v_mov_b32_e32 v137, v132
	s_add_i32 m0, s45, 0x2000
	s_add_u32 s46, s20, 0x40000
	global_load_lds_dwordx4 v137, s[20:21]
	s_addc_u32 s47, s21, 0
	v_mov_b32_e32 v137, v130
	s_add_i32 s45, s48, s28
	s_mov_b32 m0, s45
	s_nop 0
	global_load_lds_dwordx4 v137, s[46:47]
	v_mov_b32_e32 v137, v132
	s_add_i32 m0, s45, 0x2000
	s_nop 0
	global_load_lds_dwordx4 v137, s[46:47]
	v_mov_b32_e32 v137, v1
	s_mov_b32 m0, s7
	s_nop 0
	global_load_lds_dwordx4 v137, s[18:19]
	v_mov_b32_e32 v137, v131
	s_mov_b32 m0, s29
	s_nop 0
	global_load_lds_dwordx4 v137, s[18:19]
	s_waitcnt vmcnt(8)
	s_waitcnt lgkmcnt(0)
	s_barrier
	s_setprio 1
	s_waitcnt lgkmcnt(0)
	s_cmp_eq_u32 s44, -2
	s_cbranch_scc1 .Lmy_zbb_1
	v_mfma_f32_16x16x32_bf16 v[66:69], v[138:141], v[176:179], v[66:69]
	v_mfma_f32_16x16x32_bf16 v[58:61], v[146:149], v[176:179], v[58:61]
	v_mfma_f32_16x16x32_bf16 v[54:57], v[138:141], v[200:203], v[54:57]
	v_mfma_f32_16x16x32_bf16 v[50:53], v[146:149], v[200:203], v[50:53]
	v_mfma_f32_16x16x32_bf16 v[38:41], v[138:141], v[208:211], v[38:41]
	v_mfma_f32_16x16x32_bf16 v[34:37], v[146:149], v[208:211], v[34:37]
	v_mfma_f32_16x16x32_bf16 v[22:25], v[138:141], v[216:219], v[22:25]
	v_mfma_f32_16x16x32_bf16 v[18:21], v[146:149], v[216:219], v[18:21]
	v_mfma_f32_16x16x32_bf16 v[66:69], v[142:145], v[180:183], v[66:69]
	v_mfma_f32_16x16x32_bf16 v[58:61], v[150:153], v[180:183], v[58:61]
	v_mfma_f32_16x16x32_bf16 v[54:57], v[142:145], v[204:207], v[54:57]
	v_mfma_f32_16x16x32_bf16 v[50:53], v[150:153], v[204:207], v[50:53]
	v_mfma_f32_16x16x32_bf16 v[38:41], v[142:145], v[212:215], v[38:41]
	v_mfma_f32_16x16x32_bf16 v[34:37], v[150:153], v[212:215], v[34:37]
	v_mfma_f32_16x16x32_bf16 v[22:25], v[142:145], v[220:223], v[22:25]
	v_mfma_f32_16x16x32_bf16 v[18:21], v[150:153], v[220:223], v[18:21]
	s_setprio 0
	s_setprio 1
	v_mfma_f32_16x16x32_bf16 v[46:49], v[154:157], v[176:179], v[46:49]
	v_mfma_f32_16x16x32_bf16 v[42:45], v[162:165], v[176:179], v[42:45]
	v_mfma_f32_16x16x32_bf16 v[30:33], v[154:157], v[200:203], v[30:33]
	v_mfma_f32_16x16x32_bf16 v[26:29], v[162:165], v[200:203], v[26:29]
	v_mfma_f32_16x16x32_bf16 v[14:17], v[154:157], v[208:211], v[14:17]
	v_mfma_f32_16x16x32_bf16 v[10:13], v[162:165], v[208:211], v[10:13]
	v_mfma_f32_16x16x32_bf16 v[6:9], v[154:157], v[216:219], v[6:9]
	v_mfma_f32_16x16x32_bf16 v[2:5], v[162:165], v[216:219], v[2:5]
	v_mfma_f32_16x16x32_bf16 v[46:49], v[158:161], v[180:183], v[46:49]
	v_mfma_f32_16x16x32_bf16 v[42:45], v[172:175], v[180:183], v[42:45]
	v_mfma_f32_16x16x32_bf16 v[30:33], v[158:161], v[204:207], v[30:33]
	v_mfma_f32_16x16x32_bf16 v[26:29], v[172:175], v[204:207], v[26:29]
	v_mfma_f32_16x16x32_bf16 v[14:17], v[158:161], v[212:215], v[14:17]
	v_mfma_f32_16x16x32_bf16 v[10:13], v[172:175], v[212:215], v[10:13]
	v_mfma_f32_16x16x32_bf16 v[6:9], v[158:161], v[220:223], v[6:9]
	v_mfma_f32_16x16x32_bf16 v[2:5], v[172:175], v[220:223], v[2:5]
.Lmy_zbjb_1:
	s_setprio 0
	s_barrier
	s_add_i32 s45, 0, 0x18000
	v_add_u32_e32 v137, s45, v134
	s_add_i32 s48, 0, 0x1c000
	ds_read_b128 v[138:141], v137
	ds_read_b128 v[142:145], v137 offset:1024
	ds_read_b128 v[146:149], v137 offset:2048
	ds_read_b128 v[150:153], v137 offset:3072
	v_add_u32_e32 v137, s48, v134
	ds_read_b128 v[154:157], v137
	ds_read_b128 v[158:161], v137 offset:1024
	ds_read_b128 v[162:165], v137 offset:2048
	ds_read_b128 v[172:175], v137 offset:3072
	s_add_u32 s46, s18, 0x40000
	v_mov_b32_e32 v137, v1
	s_mov_b32 m0, s30
	ds_read_b128 v[176:179], v136 offset:32768
	ds_read_b128 v[180:183], v136 offset:33792
	ds_read_b128 v[200:203], v136 offset:34816
	ds_read_b128 v[204:207], v136 offset:35840
	ds_read_b128 v[208:211], v136 offset:36864
	ds_read_b128 v[212:215], v136 offset:37888
	ds_read_b128 v[216:219], v136 offset:38912
	ds_read_b128 v[220:223], v136 offset:39936
	s_addc_u32 s47, s19, 0
	s_nop 0
	global_load_lds_dwordx4 v137, s[46:47]
	v_mov_b32_e32 v137, v131
	s_mov_b32 m0, s31
	s_nop 0
	global_load_lds_dwordx4 v137, s[46:47]
	s_waitcnt vmcnt(8)
	s_waitcnt lgkmcnt(0)
	s_barrier
	s_setprio 1
	s_waitcnt lgkmcnt(0)
	v_mfma_f32_16x16x32_bf16 v[126:129], v[138:141], v[176:179], v[126:129]
	v_mfma_f32_16x16x32_bf16 v[122:125], v[146:149], v[176:179], v[122:125]
	v_mfma_f32_16x16x32_bf16 v[118:121], v[138:141], v[200:203], v[118:121]
	v_mfma_f32_16x16x32_bf16 v[114:117], v[146:149], v[200:203], v[114:117]
	v_mfma_f32_16x16x32_bf16 v[102:105], v[138:141], v[208:211], v[102:105]
	v_mfma_f32_16x16x32_bf16 v[98:101], v[146:149], v[208:211], v[98:101]
	v_mfma_f32_16x16x32_bf16 v[86:89], v[138:141], v[216:219], v[86:89]
	v_mfma_f32_16x16x32_bf16 v[82:85], v[146:149], v[216:219], v[82:85]
	v_mfma_f32_16x16x32_bf16 v[126:129], v[142:145], v[180:183], v[126:129]
	v_mfma_f32_16x16x32_bf16 v[122:125], v[150:153], v[180:183], v[122:125]
	v_mfma_f32_16x16x32_bf16 v[118:121], v[142:145], v[204:207], v[118:121]
	v_mfma_f32_16x16x32_bf16 v[114:117], v[150:153], v[204:207], v[114:117]
	v_mfma_f32_16x16x32_bf16 v[102:105], v[142:145], v[212:215], v[102:105]
	v_mfma_f32_16x16x32_bf16 v[98:101], v[150:153], v[212:215], v[98:101]
	v_mfma_f32_16x16x32_bf16 v[86:89], v[142:145], v[220:223], v[86:89]
	v_mfma_f32_16x16x32_bf16 v[82:85], v[150:153], v[220:223], v[82:85]
	s_setprio 0
	s_setprio 1
	v_mfma_f32_16x16x32_bf16 v[110:113], v[154:157], v[176:179], v[110:113]
	v_mfma_f32_16x16x32_bf16 v[106:109], v[162:165], v[176:179], v[106:109]
	v_mfma_f32_16x16x32_bf16 v[94:97], v[154:157], v[200:203], v[94:97]
	v_mfma_f32_16x16x32_bf16 v[90:93], v[162:165], v[200:203], v[90:93]
	v_mfma_f32_16x16x32_bf16 v[78:81], v[154:157], v[208:211], v[78:81]
	v_mfma_f32_16x16x32_bf16 v[74:77], v[162:165], v[208:211], v[74:77]
	v_mfma_f32_16x16x32_bf16 v[70:73], v[154:157], v[216:219], v[70:73]
	v_mfma_f32_16x16x32_bf16 v[62:65], v[162:165], v[216:219], v[62:65]
	v_mfma_f32_16x16x32_bf16 v[110:113], v[158:161], v[180:183], v[110:113]
	v_mfma_f32_16x16x32_bf16 v[106:109], v[172:175], v[180:183], v[106:109]
	v_mfma_f32_16x16x32_bf16 v[94:97], v[158:161], v[204:207], v[94:97]
	v_mfma_f32_16x16x32_bf16 v[90:93], v[172:175], v[204:207], v[90:93]
	v_mfma_f32_16x16x32_bf16 v[78:81], v[158:161], v[212:215], v[78:81]
	v_mfma_f32_16x16x32_bf16 v[74:77], v[172:175], v[212:215], v[74:77]
	v_mfma_f32_16x16x32_bf16 v[70:73], v[158:161], v[220:223], v[70:73]
	v_mfma_f32_16x16x32_bf16 v[62:65], v[172:175], v[220:223], v[62:65]
	s_setprio 0
	s_barrier
	v_mov_b32_e32 v166, v130
	ds_read_b128 v[176:179], v136 offset:49152
	ds_read_b128 v[180:183], v136 offset:50176
	ds_read_b128 v[200:203], v136 offset:51200
	ds_read_b128 v[204:207], v136 offset:52224
	ds_read_b128 v[208:211], v136 offset:53248
	ds_read_b128 v[212:215], v136 offset:54272
	ds_read_b128 v[216:219], v136 offset:55296
	ds_read_b128 v[220:223], v136 offset:56320
	s_add_i32 s45, s45, s28
	v_lshl_add_u64 v[184:185], s[20:21], 0, v[166:167]
	v_lshl_add_u64 v[184:185], v[184:185], 0, s[80:81]
	s_mov_b32 m0, s45
	v_mov_b32_e32 v166, v132
	global_load_lds_dwordx4 v[184:185], off
	s_add_i32 m0, s45, 0x2000
	v_mov_b32_e32 v137, v130
	v_lshl_add_u64 v[184:185], s[20:21], 0, v[166:167]
	s_add_u32 s20, s20, 0x40080
	v_lshl_add_u64 v[184:185], v[184:185], 0, s[80:81]
	s_addc_u32 s21, s21, 0
	s_add_i32 s45, s48, s28
	global_load_lds_dwordx4 v[184:185], off
	s_mov_b32 m0, s45
	v_mov_b32_e32 v166, v1
	global_load_lds_dwordx4 v137, s[20:21]
	v_mov_b32_e32 v137, v132
	s_add_i32 m0, s45, 0x2000
	s_nop 0
	global_load_lds_dwordx4 v137, s[20:21]
	s_mov_b32 m0, s34
	v_lshl_add_u64 v[184:185], s[18:19], 0, v[166:167]
	v_lshl_add_u64 v[184:185], v[184:185], 0, s[80:81]
	v_mov_b32_e32 v166, v131
	global_load_lds_dwordx4 v[184:185], off
	s_mov_b32 m0, s35
	v_lshl_add_u64 v[184:185], s[18:19], 0, v[166:167]
	v_lshl_add_u64 v[184:185], v[184:185], 0, s[80:81]
	global_load_lds_dwordx4 v[184:185], off
	s_waitcnt vmcnt(8)
	s_waitcnt lgkmcnt(0)
	s_barrier
	s_setprio 1
	s_waitcnt lgkmcnt(0)
	v_mfma_f32_16x16x32_bf16 v[66:69], v[138:141], v[176:179], v[66:69]
	v_mfma_f32_16x16x32_bf16 v[58:61], v[146:149], v[176:179], v[58:61]
	v_mfma_f32_16x16x32_bf16 v[54:57], v[138:141], v[200:203], v[54:57]
	v_mfma_f32_16x16x32_bf16 v[50:53], v[146:149], v[200:203], v[50:53]
	v_mfma_f32_16x16x32_bf16 v[38:41], v[138:141], v[208:211], v[38:41]
	v_mfma_f32_16x16x32_bf16 v[34:37], v[146:149], v[208:211], v[34:37]
	v_mfma_f32_16x16x32_bf16 v[22:25], v[138:141], v[216:219], v[22:25]
	v_mfma_f32_16x16x32_bf16 v[18:21], v[146:149], v[216:219], v[18:21]
	v_mfma_f32_16x16x32_bf16 v[66:69], v[142:145], v[180:183], v[66:69]
	v_mfma_f32_16x16x32_bf16 v[58:61], v[150:153], v[180:183], v[58:61]
	v_mfma_f32_16x16x32_bf16 v[54:57], v[142:145], v[204:207], v[54:57]
	v_mfma_f32_16x16x32_bf16 v[50:53], v[150:153], v[204:207], v[50:53]
	v_mfma_f32_16x16x32_bf16 v[38:41], v[142:145], v[212:215], v[38:41]
	v_mfma_f32_16x16x32_bf16 v[34:37], v[150:153], v[212:215], v[34:37]
	v_mfma_f32_16x16x32_bf16 v[22:25], v[142:145], v[220:223], v[22:25]
	v_mfma_f32_16x16x32_bf16 v[18:21], v[150:153], v[220:223], v[18:21]
	s_setprio 0
	s_setprio 1
	v_mfma_f32_16x16x32_bf16 v[46:49], v[154:157], v[176:179], v[46:49]
	v_mfma_f32_16x16x32_bf16 v[42:45], v[162:165], v[176:179], v[42:45]
	v_mfma_f32_16x16x32_bf16 v[30:33], v[154:157], v[200:203], v[30:33]
	v_mfma_f32_16x16x32_bf16 v[26:29], v[162:165], v[200:203], v[26:29]
	v_mfma_f32_16x16x32_bf16 v[14:17], v[154:157], v[208:211], v[14:17]
	v_mfma_f32_16x16x32_bf16 v[10:13], v[162:165], v[208:211], v[10:13]
	v_mfma_f32_16x16x32_bf16 v[6:9], v[154:157], v[216:219], v[6:9]
	v_mfma_f32_16x16x32_bf16 v[2:5], v[162:165], v[216:219], v[2:5]
	v_mfma_f32_16x16x32_bf16 v[46:49], v[158:161], v[180:183], v[46:49]
	v_mfma_f32_16x16x32_bf16 v[42:45], v[172:175], v[180:183], v[42:45]
	v_mfma_f32_16x16x32_bf16 v[30:33], v[158:161], v[204:207], v[30:33]
	v_mfma_f32_16x16x32_bf16 v[26:29], v[172:175], v[204:207], v[26:29]
	v_mfma_f32_16x16x32_bf16 v[14:17], v[158:161], v[212:215], v[14:17]
	v_mfma_f32_16x16x32_bf16 v[10:13], v[172:175], v[212:215], v[10:13]
	v_mfma_f32_16x16x32_bf16 v[6:9], v[158:161], v[220:223], v[6:9]
	v_mfma_f32_16x16x32_bf16 v[2:5], v[172:175], v[220:223], v[2:5]
	s_setprio 0
	s_barrier
	s_add_i32 s44, s44, 2
	s_add_u32 s42, s42, 0x100
	s_addc_u32 s43, s43, 0
	s_add_u32 s16, s16, 0x100
	s_addc_u32 s17, s17, 0
	s_cmp_gt_u32 s44, 13
	s_cbranch_scc0 .LBB0_168
	s_and_b64 vcc, exec, s[8:9]
	s_cbranch_vccz .LBB0_171
	s_barrier

.LBB0_463:
	s_nop 9
	v_max3_f32 v206, v82, v66, s90
	v_max_f32_e32 v208, v83, v67
	v_max3_f32 v206, v206, v84, v68
	v_max3_f32 v208, v208, v85, v69
	v_max3_f32 v206, v206, v86, v70
	v_max3_f32 v208, v208, v87, v71
	v_max3_f32 v206, v206, v88, v72
	v_max3_f32 v208, v208, v89, v73
	v_max3_f32 v206, v206, v90, v74
	v_max3_f32 v208, v208, v91, v75
	v_max3_f32 v206, v206, v92, v76
	v_max3_f32 v208, v208, v93, v77
	v_max3_f32 v206, v206, v94, v78
	v_max3_f32 v208, v208, v95, v79
	v_max3_f32 v206, v206, v96, v80
	v_max3_f32 v208, v208, v97, v81
	v_max_f32_e32 v206, v206, v208
	v_mov_b32_e32 v208, v206
	v_mov_b32_e32 v209, v206
	s_nop 1
	v_permlane32_swap_b32_e32 v208, v209
	v_max3_f32 v206, v207, v208, v209
	v_cmp_neq_f32_e32 vcc, v206, v207
	s_cbranch_vccz .LBB0_465
	v_sub_f32_e32 v207, v207, v206
	v_mul_f32_e32 v207, 0x3dd53b94, v207
	v_exp_f32_e32 v208, v207
	s_nop 0
	v_pk_mul_f32 v[64:65], v[64:65], v[208:209] op_sel_hi:[1,0]
	v_pk_mul_f32 v[62:63], v[62:63], v[208:209] op_sel_hi:[1,0]
	v_pk_mul_f32 v[60:61], v[60:61], v[208:209] op_sel_hi:[1,0]
	v_pk_mul_f32 v[58:59], v[58:59], v[208:209] op_sel_hi:[1,0]
	v_pk_mul_f32 v[56:57], v[56:57], v[208:209] op_sel_hi:[1,0]
	v_pk_mul_f32 v[54:55], v[54:55], v[208:209] op_sel_hi:[1,0]
	v_pk_mul_f32 v[52:53], v[52:53], v[208:209] op_sel_hi:[1,0]
	v_pk_mul_f32 v[50:51], v[50:51], v[208:209] op_sel_hi:[1,0]
	v_pk_mul_f32 v[48:49], v[48:49], v[208:209] op_sel_hi:[1,0]
	v_pk_mul_f32 v[46:47], v[46:47], v[208:209] op_sel_hi:[1,0]
	v_pk_mul_f32 v[44:45], v[44:45], v[208:209] op_sel_hi:[1,0]
	v_pk_mul_f32 v[42:43], v[42:43], v[208:209] op_sel_hi:[1,0]
	v_pk_mul_f32 v[40:41], v[40:41], v[208:209] op_sel_hi:[1,0]
	v_pk_mul_f32 v[38:39], v[38:39], v[208:209] op_sel_hi:[1,0]
	v_pk_mul_f32 v[36:37], v[36:37], v[208:209] op_sel_hi:[1,0]
	v_pk_mul_f32 v[34:35], v[34:35], v[208:209] op_sel_hi:[1,0]
	v_pk_mul_f32 v[32:33], v[32:33], v[208:209] op_sel_hi:[1,0]
	v_pk_mul_f32 v[30:31], v[30:31], v[208:209] op_sel_hi:[1,0]
	v_pk_mul_f32 v[28:29], v[28:29], v[208:209] op_sel_hi:[1,0]
	v_pk_mul_f32 v[26:27], v[26:27], v[208:209] op_sel_hi:[1,0]
	v_pk_mul_f32 v[24:25], v[24:25], v[208:209] op_sel_hi:[1,0]
	v_pk_mul_f32 v[22:23], v[22:23], v[208:209] op_sel_hi:[1,0]
	v_pk_mul_f32 v[20:21], v[20:21], v[208:209] op_sel_hi:[1,0]
	v_pk_mul_f32 v[18:19], v[18:19], v[208:209] op_sel_hi:[1,0]
	v_pk_mul_f32 v[16:17], v[16:17], v[208:209] op_sel_hi:[1,0]
	v_pk_mul_f32 v[14:15], v[14:15], v[208:209] op_sel_hi:[1,0]
	v_pk_mul_f32 v[12:13], v[12:13], v[208:209] op_sel_hi:[1,0]
	v_pk_mul_f32 v[10:11], v[10:11], v[208:209] op_sel_hi:[1,0]
	v_pk_mul_f32 v[8:9], v[8:9], v[208:209] op_sel_hi:[1,0]
	v_pk_mul_f32 v[6:7], v[6:7], v[208:209] op_sel_hi:[1,0]
	v_pk_mul_f32 v[4:5], v[4:5], v[208:209] op_sel_hi:[1,0]
	v_pk_mul_f32 v[2:3], v[2:3], v[208:209] op_sel_hi:[1,0]
	v_mul_f32_e32 v205, v205, v208
.LBB0_465:
	v_mul_f32_e32 v207, 0xbdd53b94, v206
	v_fmamk_f32 v82, v82, 0x3dd53b94, v207
	v_fmamk_f32 v66, v66, 0x3dd53b94, v207
	v_exp_f32_e32 v82, v82
	v_exp_f32_e32 v208, v66
	v_fmamk_f32 v66, v83, 0x3dd53b94, v207
	v_fmamk_f32 v67, v67, 0x3dd53b94, v207
	v_exp_f32_e32 v66, v66
	v_exp_f32_e32 v83, v67
	v_fmamk_f32 v84, v84, 0x3dd53b94, v207
	v_fmamk_f32 v68, v68, 0x3dd53b94, v207
	v_add_f32_e32 v67, v82, v208
	v_exp_f32_e32 v84, v84
	v_exp_f32_e32 v210, v68
	v_fmamk_f32 v68, v85, 0x3dd53b94, v207
	v_fmamk_f32 v69, v69, 0x3dd53b94, v207
	v_add_f32_e32 v209, v66, v83
	v_exp_f32_e32 v68, v68
	v_exp_f32_e32 v85, v69
	v_fmamk_f32 v86, v86, 0x3dd53b94, v207
	v_fmamk_f32 v70, v70, 0x3dd53b94, v207
	v_add_f32_e32 v67, v209, v67
	v_exp_f32_e32 v86, v86
	v_exp_f32_e32 v209, v70
	v_fmamk_f32 v70, v87, 0x3dd53b94, v207
	v_fmamk_f32 v71, v71, 0x3dd53b94, v207
	v_exp_f32_e32 v70, v70
	v_exp_f32_e32 v87, v71
	v_fmamk_f32 v71, v88, 0x3dd53b94, v207
	v_fmamk_f32 v72, v72, 0x3dd53b94, v207
	v_add_f32_e32 v69, v84, v210
	v_exp_f32_e32 v71, v71
	v_exp_f32_e32 v88, v72
	v_fmamk_f32 v72, v89, 0x3dd53b94, v207
	v_fmamk_f32 v73, v73, 0x3dd53b94, v207
	v_add_f32_e32 v67, v69, v67
	v_add_f32_e32 v69, v68, v85
	v_exp_f32_e32 v72, v72
	v_exp_f32_e32 v89, v73
	v_fmamk_f32 v73, v90, 0x3dd53b94, v207
	v_fmamk_f32 v74, v74, 0x3dd53b94, v207
	v_add_f32_e32 v67, v69, v67
	v_add_f32_e32 v69, v86, v209
	v_exp_f32_e32 v73, v73
	v_exp_f32_e32 v90, v74
	v_fmamk_f32 v74, v91, 0x3dd53b94, v207
	v_fmamk_f32 v75, v75, 0x3dd53b94, v207
	v_add_f32_e32 v67, v69, v67
	v_add_f32_e32 v69, v70, v87
	v_exp_f32_e32 v74, v74
	v_exp_f32_e32 v91, v75
	v_fmamk_f32 v75, v92, 0x3dd53b94, v207
	v_fmamk_f32 v76, v76, 0x3dd53b94, v207
	v_add_f32_e32 v67, v69, v67
	v_add_f32_e32 v69, v71, v88
	v_exp_f32_e32 v75, v75
	v_exp_f32_e32 v92, v76
	v_fmamk_f32 v76, v93, 0x3dd53b94, v207
	v_fmamk_f32 v77, v77, 0x3dd53b94, v207
	v_add_f32_e32 v67, v69, v67
	v_add_f32_e32 v69, v72, v89
	v_exp_f32_e32 v76, v76
	v_exp_f32_e32 v93, v77
	v_fmamk_f32 v77, v94, 0x3dd53b94, v207
	v_fmamk_f32 v78, v78, 0x3dd53b94, v207
	v_add_f32_e32 v67, v69, v67
	v_add_f32_e32 v69, v73, v90
	v_exp_f32_e32 v77, v77
	v_exp_f32_e32 v94, v78
	v_fmamk_f32 v78, v95, 0x3dd53b94, v207
	v_fmamk_f32 v79, v79, 0x3dd53b94, v207
	v_add_f32_e32 v67, v69, v67
	v_add_f32_e32 v69, v74, v91
	v_exp_f32_e32 v78, v78
	v_exp_f32_e32 v95, v79
	v_fmamk_f32 v79, v96, 0x3dd53b94, v207
	v_fmamk_f32 v80, v80, 0x3dd53b94, v207
	v_add_f32_e32 v67, v69, v67
	v_add_f32_e32 v69, v75, v92
	v_exp_f32_e32 v79, v79
	v_exp_f32_e32 v96, v80
	v_fmamk_f32 v80, v97, 0x3dd53b94, v207
	v_fmac_f32_e32 v207, 0x3dd53b94, v81
	v_add_f32_e32 v67, v69, v67
	v_add_f32_e32 v69, v76, v93
	v_exp_f32_e32 v80, v80
	v_exp_f32_e32 v81, v207
	v_add_f32_e32 v67, v69, v67
	v_add_f32_e32 v69, v77, v94
	v_add_f32_e32 v67, v69, v67
	v_add_f32_e32 v69, v78, v95
	v_add_f32_e32 v67, v69, v67
	v_add_f32_e32 v69, v79, v96
	v_add_f32_e32 v67, v69, v67
	v_add_f32_e32 v69, v80, v81
	s_mul_i32 s48, s47, 0x5000
	v_add_f32_e32 v97, v69, v67
	v_cvt_pk_bf16_f32 v69, v71, v72
	v_cvt_pk_bf16_f32 v72, v77, v78
	v_cvt_pk_bf16_f32 v78, v90, v91
	v_add_u32_e32 v90, s48, v204
	v_cvt_pk_bf16_f32 v66, v82, v66
	v_cvt_pk_bf16_f32 v67, v84, v68
	v_cvt_pk_bf16_f32 v68, v86, v70
	v_cvt_pk_bf16_f32 v70, v73, v74
	v_cvt_pk_bf16_f32 v71, v75, v76
	v_cvt_pk_bf16_f32 v74, v208, v83
	v_cvt_pk_bf16_f32 v75, v210, v85
	v_cvt_pk_bf16_f32 v76, v209, v87
	v_cvt_pk_bf16_f32 v77, v88, v89
	ds_read_b128 v[82:85], v90 offset:53248
	ds_read_b128 v[86:89], v90 offset:58368
	v_cvt_pk_bf16_f32 v73, v79, v80
	v_cvt_pk_bf16_f32 v79, v92, v93
	v_cvt_pk_bf16_f32 v80, v94, v95
	v_cvt_pk_bf16_f32 v81, v96, v81
	v_add_u32_e32 v91, 0xd000, v90
	s_waitcnt lgkmcnt(1)
	v_mfma_f32_32x32x16_bf16 v[50:65], v[82:85], v[66:69], v[50:65]
	ds_read_b128 v[82:85], v90 offset:63488
	s_waitcnt lgkmcnt(1)
	v_mfma_f32_32x32x16_bf16 v[34:49], v[86:89], v[66:69], v[34:49]
	ds_read_b128 v[86:89], v91 offset:15360
	s_waitcnt lgkmcnt(1)
	v_mfma_f32_32x32x16_bf16 v[18:33], v[82:85], v[66:69], v[18:33]
	ds_read_b128 v[82:85], v90 offset:53264
	s_waitcnt lgkmcnt(1)
	v_mfma_f32_32x32x16_bf16 v[2:17], v[86:89], v[66:69], v[2:17]
	ds_read_b128 v[66:69], v90 offset:58384
	s_waitcnt lgkmcnt(1)
	v_mfma_f32_32x32x16_bf16 v[50:65], v[82:85], v[70:73], v[50:65]
	ds_read_b128 v[82:85], v90 offset:63504
	s_waitcnt lgkmcnt(1)
	v_mfma_f32_32x32x16_bf16 v[34:49], v[66:69], v[70:73], v[34:49]
	ds_read_b128 v[66:69], v91 offset:15376
	s_waitcnt lgkmcnt(1)
	v_mfma_f32_32x32x16_bf16 v[18:33], v[82:85], v[70:73], v[18:33]
	ds_read_b128 v[82:85], v90 offset:53312
	s_waitcnt lgkmcnt(1)
	v_mfma_f32_32x32x16_bf16 v[2:17], v[66:69], v[70:73], v[2:17]
	ds_read_b128 v[66:69], v90 offset:58432
	s_waitcnt lgkmcnt(1)
	v_mfma_f32_32x32x16_bf16 v[50:65], v[82:85], v[74:77], v[50:65]
	ds_read_b128 v[70:73], v90 offset:63552
	s_waitcnt lgkmcnt(1)
	v_mfma_f32_32x32x16_bf16 v[34:49], v[66:69], v[74:77], v[34:49]
	ds_read_b128 v[66:69], v91 offset:15424
	s_waitcnt lgkmcnt(1)
	v_mfma_f32_32x32x16_bf16 v[18:33], v[70:73], v[74:77], v[18:33]
	ds_read_b128 v[70:73], v90 offset:53328
	s_waitcnt lgkmcnt(1)
	v_mfma_f32_32x32x16_bf16 v[2:17], v[66:69], v[74:77], v[2:17]
	ds_read_b128 v[66:69], v90 offset:58448
	s_waitcnt lgkmcnt(1)
	v_mfma_f32_32x32x16_bf16 v[50:65], v[70:73], v[78:81], v[50:65]
	ds_read_b128 v[70:73], v90 offset:63568
	s_waitcnt lgkmcnt(1)
	v_mfma_f32_32x32x16_bf16 v[34:49], v[66:69], v[78:81], v[34:49]
	ds_read_b128 v[66:69], v91 offset:15440
	s_waitcnt lgkmcnt(1)
	v_mfma_f32_32x32x16_bf16 v[18:33], v[70:73], v[78:81], v[18:33]
	s_waitcnt lgkmcnt(0)
	v_mfma_f32_32x32x16_bf16 v[2:17], v[66:69], v[78:81], v[2:17]
	v_add_f32_e32 v205, v97, v205
	s_andn2_b64 vcc, exec, s[26:27]
	s_cbranch_vccz .LBB0_467
	s_branch .LBB0_468

.LBB0_476:
	s_nop 9
	v_max3_f32 v207, v82, v66, s90
	v_max_f32_e32 v209, v83, v67
	v_max3_f32 v207, v207, v84, v68
	v_max3_f32 v209, v209, v85, v69
	v_max3_f32 v207, v207, v86, v70
	v_max3_f32 v209, v209, v87, v71
	v_max3_f32 v207, v207, v88, v72
	v_max3_f32 v209, v209, v89, v73
	v_max3_f32 v207, v207, v90, v74
	v_max3_f32 v209, v209, v91, v75
	v_max3_f32 v207, v207, v92, v76
	v_max3_f32 v209, v209, v93, v77
	v_max3_f32 v207, v207, v94, v78
	v_max3_f32 v209, v209, v95, v79
	v_max3_f32 v207, v207, v96, v80
	v_max3_f32 v209, v209, v97, v81
	v_max_f32_e32 v207, v207, v209
	v_mov_b32_e32 v209, v207
	v_mov_b32_e32 v210, v207
	s_nop 1
	v_permlane32_swap_b32_e32 v209, v210
	v_max3_f32 v207, v208, v209, v210
	v_cmp_neq_f32_e32 vcc, v207, v208
	s_cbranch_vccz .LBB0_478
	v_sub_f32_e32 v208, v208, v207
	v_mul_f32_e32 v208, 0x3dd53b94, v208
	v_exp_f32_e32 v208, v208
	s_nop 0
	v_pk_mul_f32 v[64:65], v[64:65], v[208:209] op_sel_hi:[1,0]
	v_pk_mul_f32 v[62:63], v[62:63], v[208:209] op_sel_hi:[1,0]
	v_pk_mul_f32 v[60:61], v[60:61], v[208:209] op_sel_hi:[1,0]
	v_pk_mul_f32 v[58:59], v[58:59], v[208:209] op_sel_hi:[1,0]
	v_pk_mul_f32 v[56:57], v[56:57], v[208:209] op_sel_hi:[1,0]
	v_pk_mul_f32 v[54:55], v[54:55], v[208:209] op_sel_hi:[1,0]
	v_pk_mul_f32 v[52:53], v[52:53], v[208:209] op_sel_hi:[1,0]
	v_pk_mul_f32 v[50:51], v[50:51], v[208:209] op_sel_hi:[1,0]
	v_pk_mul_f32 v[48:49], v[48:49], v[208:209] op_sel_hi:[1,0]
	v_pk_mul_f32 v[46:47], v[46:47], v[208:209] op_sel_hi:[1,0]
	v_pk_mul_f32 v[44:45], v[44:45], v[208:209] op_sel_hi:[1,0]
	v_pk_mul_f32 v[42:43], v[42:43], v[208:209] op_sel_hi:[1,0]
	v_pk_mul_f32 v[40:41], v[40:41], v[208:209] op_sel_hi:[1,0]
	v_pk_mul_f32 v[38:39], v[38:39], v[208:209] op_sel_hi:[1,0]
	v_pk_mul_f32 v[36:37], v[36:37], v[208:209] op_sel_hi:[1,0]
	v_pk_mul_f32 v[34:35], v[34:35], v[208:209] op_sel_hi:[1,0]
	v_pk_mul_f32 v[32:33], v[32:33], v[208:209] op_sel_hi:[1,0]
	v_pk_mul_f32 v[30:31], v[30:31], v[208:209] op_sel_hi:[1,0]
	v_pk_mul_f32 v[28:29], v[28:29], v[208:209] op_sel_hi:[1,0]
	v_pk_mul_f32 v[26:27], v[26:27], v[208:209] op_sel_hi:[1,0]
	v_pk_mul_f32 v[24:25], v[24:25], v[208:209] op_sel_hi:[1,0]
	v_pk_mul_f32 v[22:23], v[22:23], v[208:209] op_sel_hi:[1,0]
	v_pk_mul_f32 v[20:21], v[20:21], v[208:209] op_sel_hi:[1,0]
	v_pk_mul_f32 v[18:19], v[18:19], v[208:209] op_sel_hi:[1,0]
	v_pk_mul_f32 v[16:17], v[16:17], v[208:209] op_sel_hi:[1,0]
	v_pk_mul_f32 v[14:15], v[14:15], v[208:209] op_sel_hi:[1,0]
	v_pk_mul_f32 v[12:13], v[12:13], v[208:209] op_sel_hi:[1,0]
	v_pk_mul_f32 v[10:11], v[10:11], v[208:209] op_sel_hi:[1,0]
	v_pk_mul_f32 v[8:9], v[8:9], v[208:209] op_sel_hi:[1,0]
	v_pk_mul_f32 v[6:7], v[6:7], v[208:209] op_sel_hi:[1,0]
	v_pk_mul_f32 v[4:5], v[4:5], v[208:209] op_sel_hi:[1,0]
	v_pk_mul_f32 v[2:3], v[2:3], v[208:209] op_sel_hi:[1,0]
	v_mul_f32_e32 v205, v205, v208
.LBB0_478:
	v_mul_f32_e32 v208, 0xbdd53b94, v207
	v_fmamk_f32 v82, v82, 0x3dd53b94, v208
	v_fmamk_f32 v66, v66, 0x3dd53b94, v208
	v_exp_f32_e32 v82, v82
	v_exp_f32_e32 v209, v66
	v_fmamk_f32 v66, v83, 0x3dd53b94, v208
	v_fmamk_f32 v67, v67, 0x3dd53b94, v208
	v_exp_f32_e32 v66, v66
	v_exp_f32_e32 v83, v67
	v_fmamk_f32 v84, v84, 0x3dd53b94, v208
	v_fmamk_f32 v68, v68, 0x3dd53b94, v208
	v_add_f32_e32 v67, v82, v209
	v_exp_f32_e32 v84, v84
	v_exp_f32_e32 v211, v68
	v_fmamk_f32 v68, v85, 0x3dd53b94, v208
	v_fmamk_f32 v69, v69, 0x3dd53b94, v208
	v_add_f32_e32 v210, v66, v83
	v_exp_f32_e32 v68, v68
	v_exp_f32_e32 v85, v69
	v_fmamk_f32 v86, v86, 0x3dd53b94, v208
	v_fmamk_f32 v70, v70, 0x3dd53b94, v208
	v_add_f32_e32 v67, v210, v67
	v_exp_f32_e32 v86, v86
	v_exp_f32_e32 v210, v70
	v_fmamk_f32 v70, v87, 0x3dd53b94, v208
	v_fmamk_f32 v71, v71, 0x3dd53b94, v208
	v_exp_f32_e32 v70, v70
	v_exp_f32_e32 v87, v71
	v_fmamk_f32 v71, v88, 0x3dd53b94, v208
	v_fmamk_f32 v72, v72, 0x3dd53b94, v208
	v_add_f32_e32 v69, v84, v211
	v_exp_f32_e32 v71, v71
	v_exp_f32_e32 v88, v72
	v_fmamk_f32 v72, v89, 0x3dd53b94, v208
	v_fmamk_f32 v73, v73, 0x3dd53b94, v208
	v_add_f32_e32 v67, v69, v67
	v_add_f32_e32 v69, v68, v85
	v_exp_f32_e32 v72, v72
	v_exp_f32_e32 v89, v73
	v_fmamk_f32 v73, v90, 0x3dd53b94, v208
	v_fmamk_f32 v74, v74, 0x3dd53b94, v208
	v_add_f32_e32 v67, v69, v67
	v_add_f32_e32 v69, v86, v210
	v_exp_f32_e32 v73, v73
	v_exp_f32_e32 v90, v74
	v_fmamk_f32 v74, v91, 0x3dd53b94, v208
	v_fmamk_f32 v75, v75, 0x3dd53b94, v208
	v_add_f32_e32 v67, v69, v67
	v_add_f32_e32 v69, v70, v87
	v_exp_f32_e32 v74, v74
	v_exp_f32_e32 v91, v75
	v_fmamk_f32 v75, v92, 0x3dd53b94, v208
	v_fmamk_f32 v76, v76, 0x3dd53b94, v208
	v_add_f32_e32 v67, v69, v67
	v_add_f32_e32 v69, v71, v88
	v_exp_f32_e32 v75, v75
	v_exp_f32_e32 v92, v76
	v_fmamk_f32 v76, v93, 0x3dd53b94, v208
	v_fmamk_f32 v77, v77, 0x3dd53b94, v208
	v_add_f32_e32 v67, v69, v67
	v_add_f32_e32 v69, v72, v89
	v_exp_f32_e32 v76, v76
	v_exp_f32_e32 v93, v77
	v_fmamk_f32 v77, v94, 0x3dd53b94, v208
	v_fmamk_f32 v78, v78, 0x3dd53b94, v208
	v_add_f32_e32 v67, v69, v67
	v_add_f32_e32 v69, v73, v90
	v_exp_f32_e32 v77, v77
	v_exp_f32_e32 v94, v78
	v_fmamk_f32 v78, v95, 0x3dd53b94, v208
	v_fmamk_f32 v79, v79, 0x3dd53b94, v208
	v_add_f32_e32 v67, v69, v67
	v_add_f32_e32 v69, v74, v91
	v_exp_f32_e32 v78, v78
	v_exp_f32_e32 v95, v79
	v_fmamk_f32 v79, v96, 0x3dd53b94, v208
	v_fmamk_f32 v80, v80, 0x3dd53b94, v208
	v_add_f32_e32 v67, v69, v67
	v_add_f32_e32 v69, v75, v92
	v_exp_f32_e32 v79, v79
	v_exp_f32_e32 v96, v80
	v_fmamk_f32 v80, v97, 0x3dd53b94, v208
	v_fmac_f32_e32 v208, 0x3dd53b94, v81
	v_add_f32_e32 v67, v69, v67
	v_add_f32_e32 v69, v76, v93
	v_exp_f32_e32 v80, v80
	v_exp_f32_e32 v81, v208
	v_add_f32_e32 v67, v69, v67
	v_add_f32_e32 v69, v77, v94
	v_add_f32_e32 v67, v69, v67
	v_add_f32_e32 v69, v78, v95
	v_add_f32_e32 v67, v69, v67
	v_add_f32_e32 v69, v79, v96
	v_add_f32_e32 v67, v69, v67
	v_add_f32_e32 v69, v80, v81
	s_mul_i32 s22, s17, 0x5000
	v_add_f32_e32 v97, v69, v67
	v_cvt_pk_bf16_f32 v69, v71, v72
	v_cvt_pk_bf16_f32 v72, v77, v78
	v_cvt_pk_bf16_f32 v78, v90, v91
	v_add_u32_e32 v90, s22, v206
	v_cvt_pk_bf16_f32 v66, v82, v66
	v_cvt_pk_bf16_f32 v67, v84, v68
	v_cvt_pk_bf16_f32 v68, v86, v70
	v_cvt_pk_bf16_f32 v70, v73, v74
	v_cvt_pk_bf16_f32 v71, v75, v76
	v_cvt_pk_bf16_f32 v74, v209, v83
	v_cvt_pk_bf16_f32 v75, v211, v85
	v_cvt_pk_bf16_f32 v76, v210, v87
	v_cvt_pk_bf16_f32 v77, v88, v89
	ds_read_b128 v[82:85], v90 offset:53248
	ds_read_b128 v[86:89], v90 offset:58368
	v_cvt_pk_bf16_f32 v73, v79, v80
	v_cvt_pk_bf16_f32 v79, v92, v93
	v_cvt_pk_bf16_f32 v80, v94, v95
	v_cvt_pk_bf16_f32 v81, v96, v81
	v_add_u32_e32 v91, 0xd000, v90
	s_waitcnt lgkmcnt(1)
	v_mfma_f32_32x32x16_bf16 v[50:65], v[82:85], v[66:69], v[50:65]
	ds_read_b128 v[82:85], v90 offset:63488
	s_waitcnt lgkmcnt(1)
	v_mfma_f32_32x32x16_bf16 v[34:49], v[86:89], v[66:69], v[34:49]
	ds_read_b128 v[86:89], v91 offset:15360
	s_waitcnt lgkmcnt(1)
	v_mfma_f32_32x32x16_bf16 v[18:33], v[82:85], v[66:69], v[18:33]
	ds_read_b128 v[82:85], v90 offset:53264
	s_waitcnt lgkmcnt(1)
	v_mfma_f32_32x32x16_bf16 v[2:17], v[86:89], v[66:69], v[2:17]
	ds_read_b128 v[66:69], v90 offset:58384
	s_waitcnt lgkmcnt(1)
	v_mfma_f32_32x32x16_bf16 v[50:65], v[82:85], v[70:73], v[50:65]
	ds_read_b128 v[82:85], v90 offset:63504
	s_waitcnt lgkmcnt(1)
	v_mfma_f32_32x32x16_bf16 v[34:49], v[66:69], v[70:73], v[34:49]
	ds_read_b128 v[66:69], v91 offset:15376
	s_waitcnt lgkmcnt(1)
	v_mfma_f32_32x32x16_bf16 v[18:33], v[82:85], v[70:73], v[18:33]
	ds_read_b128 v[82:85], v90 offset:53312
	s_waitcnt lgkmcnt(1)
	v_mfma_f32_32x32x16_bf16 v[2:17], v[66:69], v[70:73], v[2:17]
	ds_read_b128 v[66:69], v90 offset:58432
	s_waitcnt lgkmcnt(1)
	v_mfma_f32_32x32x16_bf16 v[50:65], v[82:85], v[74:77], v[50:65]
	ds_read_b128 v[70:73], v90 offset:63552
	s_waitcnt lgkmcnt(1)
	v_mfma_f32_32x32x16_bf16 v[34:49], v[66:69], v[74:77], v[34:49]
	ds_read_b128 v[66:69], v91 offset:15424
	s_waitcnt lgkmcnt(1)
	v_mfma_f32_32x32x16_bf16 v[18:33], v[70:73], v[74:77], v[18:33]
	ds_read_b128 v[70:73], v90 offset:53328
	s_waitcnt lgkmcnt(1)
	v_mfma_f32_32x32x16_bf16 v[2:17], v[66:69], v[74:77], v[2:17]
	ds_read_b128 v[66:69], v90 offset:58448
	s_waitcnt lgkmcnt(1)
	v_mfma_f32_32x32x16_bf16 v[50:65], v[70:73], v[78:81], v[50:65]
	ds_read_b128 v[70:73], v90 offset:63568
	s_waitcnt lgkmcnt(1)
	v_mfma_f32_32x32x16_bf16 v[34:49], v[66:69], v[78:81], v[34:49]
	ds_read_b128 v[66:69], v91 offset:15440
	s_waitcnt lgkmcnt(1)
	v_mfma_f32_32x32x16_bf16 v[18:33], v[70:73], v[78:81], v[18:33]
	s_waitcnt lgkmcnt(0)
	v_mfma_f32_32x32x16_bf16 v[2:17], v[66:69], v[78:81], v[2:17]
	v_add_f32_e32 v205, v97, v205
	s_andn2_b64 vcc, exec, s[12:13]
	s_cbranch_vccz .LBB0_480
	s_branch .LBB0_481

.LBB0_556:
	s_ashr_i32 s13, s12, 31
	s_lshl_b64 s[16:17], s[12:13], 11
	s_add_u32 s16, s26, s16
	s_addc_u32 s17, s27, s17
	s_and_b64 s[22:23], s[2:3], exec
	s_cselect_b32 s13, s17, s21
	s_cselect_b32 s39, s16, s20
	s_add_u32 s40, s18, 0x100
	s_addc_u32 s41, s19, 0
	s_add_u32 s18, s20, 0x40080
	s_addc_u32 s19, s21, 0
	s_mov_b32 s42, -2
	s_branch .LBB0_557

.LBB0_557:
	s_add_u32 s20, s18, 0xfffc0080
	s_addc_u32 s21, s19, -1
	s_add_i32 s43, 0, 0x10000
	s_cmp_eq_u32 s42, 12
	s_cselect_b32 s21, s13, s21
	s_cselect_b32 s20, s39, s20
	v_add_u32_e32 v137, s43, v134
	s_cselect_b32 s23, s15, s41
	s_cselect_b32 s22, s14, s40
	s_add_i32 s46, 0, 0x14000
	ds_read_b128 v[138:141], v137
	ds_read_b128 v[142:145], v137 offset:1024
	ds_read_b128 v[146:149], v137 offset:2048
	ds_read_b128 v[150:153], v137 offset:3072
	v_add_u32_e32 v137, s46, v134
	ds_read_b128 v[154:157], v137
	ds_read_b128 v[158:161], v137 offset:1024
	ds_read_b128 v[162:165], v137 offset:2048
	ds_read_b128 v[172:175], v137 offset:3072
	v_mov_b32_e32 v137, v1
	ds_read_b128 v[176:179], v136
	ds_read_b128 v[180:183], v136 offset:1024
	ds_read_b128 v[200:203], v136 offset:2048
	ds_read_b128 v[204:207], v136 offset:3072
	ds_read_b128 v[208:211], v136 offset:4096
	ds_read_b128 v[212:215], v136 offset:5120
	ds_read_b128 v[216:219], v136 offset:6144
	ds_read_b128 v[220:223], v136 offset:7168
	s_add_i32 m0, s9, 0xc000
	s_nop 0
	global_load_lds_dwordx4 v137, s[18:19]
	v_mov_b32_e32 v137, v131
	s_add_i32 m0, s9, 0xe000
	s_nop 0
	global_load_lds_dwordx4 v137, s[18:19]
	s_waitcnt vmcnt(8)
	s_waitcnt lgkmcnt(0)
	s_barrier
	s_setprio 1
	s_waitcnt lgkmcnt(0)
	s_cmp_eq_u32 s42, -2
	s_cbranch_scc1 .Lmy_zbc_0
	v_mfma_f32_16x16x32_bf16 v[126:129], v[138:141], v[176:179], v[126:129]
	v_mfma_f32_16x16x32_bf16 v[122:125], v[146:149], v[176:179], v[122:125]
	v_mfma_f32_16x16x32_bf16 v[118:121], v[138:141], v[200:203], v[118:121]
	v_mfma_f32_16x16x32_bf16 v[114:117], v[146:149], v[200:203], v[114:117]
	v_mfma_f32_16x16x32_bf16 v[102:105], v[138:141], v[208:211], v[102:105]
	v_mfma_f32_16x16x32_bf16 v[98:101], v[146:149], v[208:211], v[98:101]
	v_mfma_f32_16x16x32_bf16 v[86:89], v[138:141], v[216:219], v[86:89]
	v_mfma_f32_16x16x32_bf16 v[82:85], v[146:149], v[216:219], v[82:85]
	v_mfma_f32_16x16x32_bf16 v[126:129], v[142:145], v[180:183], v[126:129]
	v_mfma_f32_16x16x32_bf16 v[122:125], v[150:153], v[180:183], v[122:125]
	v_mfma_f32_16x16x32_bf16 v[118:121], v[142:145], v[204:207], v[118:121]
	v_mfma_f32_16x16x32_bf16 v[114:117], v[150:153], v[204:207], v[114:117]
	v_mfma_f32_16x16x32_bf16 v[102:105], v[142:145], v[212:215], v[102:105]
	v_mfma_f32_16x16x32_bf16 v[98:101], v[150:153], v[212:215], v[98:101]
	v_mfma_f32_16x16x32_bf16 v[86:89], v[142:145], v[220:223], v[86:89]
	v_mfma_f32_16x16x32_bf16 v[82:85], v[150:153], v[220:223], v[82:85]
	s_setprio 0
	s_setprio 1
	v_mfma_f32_16x16x32_bf16 v[110:113], v[154:157], v[176:179], v[110:113]
	v_mfma_f32_16x16x32_bf16 v[106:109], v[162:165], v[176:179], v[106:109]
	v_mfma_f32_16x16x32_bf16 v[94:97], v[154:157], v[200:203], v[94:97]
	v_mfma_f32_16x16x32_bf16 v[90:93], v[162:165], v[200:203], v[90:93]
	v_mfma_f32_16x16x32_bf16 v[78:81], v[154:157], v[208:211], v[78:81]
	v_mfma_f32_16x16x32_bf16 v[74:77], v[162:165], v[208:211], v[74:77]
	v_mfma_f32_16x16x32_bf16 v[70:73], v[154:157], v[216:219], v[70:73]
	v_mfma_f32_16x16x32_bf16 v[62:65], v[162:165], v[216:219], v[62:65]
	v_mfma_f32_16x16x32_bf16 v[110:113], v[158:161], v[180:183], v[110:113]
	v_mfma_f32_16x16x32_bf16 v[106:109], v[172:175], v[180:183], v[106:109]
	v_mfma_f32_16x16x32_bf16 v[94:97], v[158:161], v[204:207], v[94:97]
	v_mfma_f32_16x16x32_bf16 v[90:93], v[172:175], v[204:207], v[90:93]
	v_mfma_f32_16x16x32_bf16 v[78:81], v[158:161], v[212:215], v[78:81]
	v_mfma_f32_16x16x32_bf16 v[74:77], v[172:175], v[212:215], v[74:77]
	v_mfma_f32_16x16x32_bf16 v[70:73], v[158:161], v[220:223], v[70:73]
	v_mfma_f32_16x16x32_bf16 v[62:65], v[172:175], v[220:223], v[62:65]
.Lmy_zbjc_0:
	s_setprio 0
	s_barrier
	v_mov_b32_e32 v137, v130
	s_add_i32 s43, s43, s28
	ds_read_b128 v[176:179], v136 offset:16384
	ds_read_b128 v[180:183], v136 offset:17408
	ds_read_b128 v[200:203], v136 offset:18432
	ds_read_b128 v[204:207], v136 offset:19456
	ds_read_b128 v[208:211], v136 offset:20480
	ds_read_b128 v[212:215], v136 offset:21504
	ds_read_b128 v[216:219], v136 offset:22528
	ds_read_b128 v[220:223], v136 offset:23552
	s_mov_b32 m0, s43
	s_nop 0
	global_load_lds_dwordx4 v137, s[22:23]
	v_mov_b32_e32 v137, v132
	s_add_i32 m0, s43, 0x2000
	s_add_u32 s44, s22, 0x40000
	global_load_lds_dwordx4 v137, s[22:23]
	s_addc_u32 s45, s23, 0
	v_mov_b32_e32 v137, v130
	s_add_i32 s43, s46, s28
	s_mov_b32 m0, s43
	s_nop 0
	global_load_lds_dwordx4 v137, s[44:45]
	v_mov_b32_e32 v137, v132
	s_add_i32 m0, s43, 0x2000
	s_nop 0
	global_load_lds_dwordx4 v137, s[44:45]
	v_mov_b32_e32 v137, v1
	s_mov_b32 m0, s9
	s_nop 0
	global_load_lds_dwordx4 v137, s[20:21]
	v_mov_b32_e32 v137, v131
	s_mov_b32 m0, s29
	s_nop 0
	global_load_lds_dwordx4 v137, s[20:21]
	s_waitcnt vmcnt(8)
	s_waitcnt lgkmcnt(0)
	s_barrier
	s_setprio 1
	s_waitcnt lgkmcnt(0)
	s_cmp_eq_u32 s42, -2
	s_cbranch_scc1 .Lmy_zbc_1
	v_mfma_f32_16x16x32_bf16 v[66:69], v[138:141], v[176:179], v[66:69]
	v_mfma_f32_16x16x32_bf16 v[58:61], v[146:149], v[176:179], v[58:61]
	v_mfma_f32_16x16x32_bf16 v[54:57], v[138:141], v[200:203], v[54:57]
	v_mfma_f32_16x16x32_bf16 v[50:53], v[146:149], v[200:203], v[50:53]
	v_mfma_f32_16x16x32_bf16 v[38:41], v[138:141], v[208:211], v[38:41]
	v_mfma_f32_16x16x32_bf16 v[34:37], v[146:149], v[208:211], v[34:37]
	v_mfma_f32_16x16x32_bf16 v[22:25], v[138:141], v[216:219], v[22:25]
	v_mfma_f32_16x16x32_bf16 v[18:21], v[146:149], v[216:219], v[18:21]
	v_mfma_f32_16x16x32_bf16 v[66:69], v[142:145], v[180:183], v[66:69]
	v_mfma_f32_16x16x32_bf16 v[58:61], v[150:153], v[180:183], v[58:61]
	v_mfma_f32_16x16x32_bf16 v[54:57], v[142:145], v[204:207], v[54:57]
	v_mfma_f32_16x16x32_bf16 v[50:53], v[150:153], v[204:207], v[50:53]
	v_mfma_f32_16x16x32_bf16 v[38:41], v[142:145], v[212:215], v[38:41]
	v_mfma_f32_16x16x32_bf16 v[34:37], v[150:153], v[212:215], v[34:37]
	v_mfma_f32_16x16x32_bf16 v[22:25], v[142:145], v[220:223], v[22:25]
	v_mfma_f32_16x16x32_bf16 v[18:21], v[150:153], v[220:223], v[18:21]
	s_setprio 0
	s_setprio 1
	v_mfma_f32_16x16x32_bf16 v[46:49], v[154:157], v[176:179], v[46:49]
	v_mfma_f32_16x16x32_bf16 v[42:45], v[162:165], v[176:179], v[42:45]
	v_mfma_f32_16x16x32_bf16 v[30:33], v[154:157], v[200:203], v[30:33]
	v_mfma_f32_16x16x32_bf16 v[26:29], v[162:165], v[200:203], v[26:29]
	v_mfma_f32_16x16x32_bf16 v[14:17], v[154:157], v[208:211], v[14:17]
	v_mfma_f32_16x16x32_bf16 v[10:13], v[162:165], v[208:211], v[10:13]
	v_mfma_f32_16x16x32_bf16 v[6:9], v[154:157], v[216:219], v[6:9]
	v_mfma_f32_16x16x32_bf16 v[2:5], v[162:165], v[216:219], v[2:5]
	v_mfma_f32_16x16x32_bf16 v[46:49], v[158:161], v[180:183], v[46:49]
	v_mfma_f32_16x16x32_bf16 v[42:45], v[172:175], v[180:183], v[42:45]
	v_mfma_f32_16x16x32_bf16 v[30:33], v[158:161], v[204:207], v[30:33]
	v_mfma_f32_16x16x32_bf16 v[26:29], v[172:175], v[204:207], v[26:29]
	v_mfma_f32_16x16x32_bf16 v[14:17], v[158:161], v[212:215], v[14:17]
	v_mfma_f32_16x16x32_bf16 v[10:13], v[172:175], v[212:215], v[10:13]
	v_mfma_f32_16x16x32_bf16 v[6:9], v[158:161], v[220:223], v[6:9]
	v_mfma_f32_16x16x32_bf16 v[2:5], v[172:175], v[220:223], v[2:5]
.Lmy_zbjc_1:
	s_setprio 0
	s_barrier
	s_add_i32 s43, 0, 0x18000
	v_add_u32_e32 v137, s43, v134
	s_add_i32 s46, 0, 0x1c000
	ds_read_b128 v[138:141], v137
	ds_read_b128 v[142:145], v137 offset:1024
	ds_read_b128 v[146:149], v137 offset:2048
	ds_read_b128 v[150:153], v137 offset:3072
	v_add_u32_e32 v137, s46, v134
	ds_read_b128 v[154:157], v137
	ds_read_b128 v[158:161], v137 offset:1024
	ds_read_b128 v[162:165], v137 offset:2048
	ds_read_b128 v[172:175], v137 offset:3072
	s_add_u32 s44, s20, 0x40000
	v_mov_b32_e32 v137, v1
	s_mov_b32 m0, s30
	ds_read_b128 v[176:179], v136 offset:32768
	ds_read_b128 v[180:183], v136 offset:33792
	ds_read_b128 v[200:203], v136 offset:34816
	ds_read_b128 v[204:207], v136 offset:35840
	ds_read_b128 v[208:211], v136 offset:36864
	ds_read_b128 v[212:215], v136 offset:37888
	ds_read_b128 v[216:219], v136 offset:38912
	ds_read_b128 v[220:223], v136 offset:39936
	s_addc_u32 s45, s21, 0
	s_nop 0
	global_load_lds_dwordx4 v137, s[44:45]
	v_mov_b32_e32 v137, v131
	s_mov_b32 m0, s31
	s_nop 0
	global_load_lds_dwordx4 v137, s[44:45]
	s_waitcnt vmcnt(8)
	s_waitcnt lgkmcnt(0)
	s_barrier
	s_setprio 1
	s_waitcnt lgkmcnt(0)
	v_mfma_f32_16x16x32_bf16 v[126:129], v[138:141], v[176:179], v[126:129]
	v_mfma_f32_16x16x32_bf16 v[122:125], v[146:149], v[176:179], v[122:125]
	v_mfma_f32_16x16x32_bf16 v[118:121], v[138:141], v[200:203], v[118:121]
	v_mfma_f32_16x16x32_bf16 v[114:117], v[146:149], v[200:203], v[114:117]
	v_mfma_f32_16x16x32_bf16 v[102:105], v[138:141], v[208:211], v[102:105]
	v_mfma_f32_16x16x32_bf16 v[98:101], v[146:149], v[208:211], v[98:101]
	v_mfma_f32_16x16x32_bf16 v[86:89], v[138:141], v[216:219], v[86:89]
	v_mfma_f32_16x16x32_bf16 v[82:85], v[146:149], v[216:219], v[82:85]
	v_mfma_f32_16x16x32_bf16 v[126:129], v[142:145], v[180:183], v[126:129]
	v_mfma_f32_16x16x32_bf16 v[122:125], v[150:153], v[180:183], v[122:125]
	v_mfma_f32_16x16x32_bf16 v[118:121], v[142:145], v[204:207], v[118:121]
	v_mfma_f32_16x16x32_bf16 v[114:117], v[150:153], v[204:207], v[114:117]
	v_mfma_f32_16x16x32_bf16 v[102:105], v[142:145], v[212:215], v[102:105]
	v_mfma_f32_16x16x32_bf16 v[98:101], v[150:153], v[212:215], v[98:101]
	v_mfma_f32_16x16x32_bf16 v[86:89], v[142:145], v[220:223], v[86:89]
	v_mfma_f32_16x16x32_bf16 v[82:85], v[150:153], v[220:223], v[82:85]
	s_setprio 0
	s_setprio 1
	v_mfma_f32_16x16x32_bf16 v[110:113], v[154:157], v[176:179], v[110:113]
	v_mfma_f32_16x16x32_bf16 v[106:109], v[162:165], v[176:179], v[106:109]
	v_mfma_f32_16x16x32_bf16 v[94:97], v[154:157], v[200:203], v[94:97]
	v_mfma_f32_16x16x32_bf16 v[90:93], v[162:165], v[200:203], v[90:93]
	v_mfma_f32_16x16x32_bf16 v[78:81], v[154:157], v[208:211], v[78:81]
	v_mfma_f32_16x16x32_bf16 v[74:77], v[162:165], v[208:211], v[74:77]
	v_mfma_f32_16x16x32_bf16 v[70:73], v[154:157], v[216:219], v[70:73]
	v_mfma_f32_16x16x32_bf16 v[62:65], v[162:165], v[216:219], v[62:65]
	v_mfma_f32_16x16x32_bf16 v[110:113], v[158:161], v[180:183], v[110:113]
	v_mfma_f32_16x16x32_bf16 v[106:109], v[172:175], v[180:183], v[106:109]
	v_mfma_f32_16x16x32_bf16 v[94:97], v[158:161], v[204:207], v[94:97]
	v_mfma_f32_16x16x32_bf16 v[90:93], v[172:175], v[204:207], v[90:93]
	v_mfma_f32_16x16x32_bf16 v[78:81], v[158:161], v[212:215], v[78:81]
	v_mfma_f32_16x16x32_bf16 v[74:77], v[172:175], v[212:215], v[74:77]
	v_mfma_f32_16x16x32_bf16 v[70:73], v[158:161], v[220:223], v[70:73]
	v_mfma_f32_16x16x32_bf16 v[62:65], v[172:175], v[220:223], v[62:65]
	s_setprio 0
	s_barrier
	v_mov_b32_e32 v166, v130
	ds_read_b128 v[176:179], v136 offset:49152
	ds_read_b128 v[180:183], v136 offset:50176
	ds_read_b128 v[200:203], v136 offset:51200
	ds_read_b128 v[204:207], v136 offset:52224
	ds_read_b128 v[208:211], v136 offset:53248
	ds_read_b128 v[212:215], v136 offset:54272
	ds_read_b128 v[216:219], v136 offset:55296
	ds_read_b128 v[220:223], v136 offset:56320
	s_add_i32 s43, s43, s28
	v_lshl_add_u64 v[184:185], s[22:23], 0, v[166:167]
	v_lshl_add_u64 v[184:185], v[184:185], 0, s[80:81]
	s_mov_b32 m0, s43
	v_mov_b32_e32 v166, v132
	global_load_lds_dwordx4 v[184:185], off
	s_add_i32 m0, s43, 0x2000
	v_mov_b32_e32 v137, v130
	v_lshl_add_u64 v[184:185], s[22:23], 0, v[166:167]
	s_add_u32 s22, s22, 0x40080
	v_lshl_add_u64 v[184:185], v[184:185], 0, s[80:81]
	s_addc_u32 s23, s23, 0
	s_add_i32 s43, s46, s28
	global_load_lds_dwordx4 v[184:185], off
	s_mov_b32 m0, s43
	v_mov_b32_e32 v166, v1
	global_load_lds_dwordx4 v137, s[22:23]
	v_mov_b32_e32 v137, v132
	s_add_i32 m0, s43, 0x2000
	s_nop 0
	global_load_lds_dwordx4 v137, s[22:23]
	s_mov_b32 m0, s34
	v_lshl_add_u64 v[184:185], s[20:21], 0, v[166:167]
	v_lshl_add_u64 v[184:185], v[184:185], 0, s[80:81]
	v_mov_b32_e32 v166, v131
	global_load_lds_dwordx4 v[184:185], off
	s_mov_b32 m0, s35
	v_lshl_add_u64 v[184:185], s[20:21], 0, v[166:167]
	v_lshl_add_u64 v[184:185], v[184:185], 0, s[80:81]
	global_load_lds_dwordx4 v[184:185], off
	s_waitcnt vmcnt(8)
	s_waitcnt lgkmcnt(0)
	s_barrier
	s_setprio 1
	s_waitcnt lgkmcnt(0)
	v_mfma_f32_16x16x32_bf16 v[66:69], v[138:141], v[176:179], v[66:69]
	v_mfma_f32_16x16x32_bf16 v[58:61], v[146:149], v[176:179], v[58:61]
	v_mfma_f32_16x16x32_bf16 v[54:57], v[138:141], v[200:203], v[54:57]
	v_mfma_f32_16x16x32_bf16 v[50:53], v[146:149], v[200:203], v[50:53]
	v_mfma_f32_16x16x32_bf16 v[38:41], v[138:141], v[208:211], v[38:41]
	v_mfma_f32_16x16x32_bf16 v[34:37], v[146:149], v[208:211], v[34:37]
	v_mfma_f32_16x16x32_bf16 v[22:25], v[138:141], v[216:219], v[22:25]
	v_mfma_f32_16x16x32_bf16 v[18:21], v[146:149], v[216:219], v[18:21]
	v_mfma_f32_16x16x32_bf16 v[66:69], v[142:145], v[180:183], v[66:69]
	v_mfma_f32_16x16x32_bf16 v[58:61], v[150:153], v[180:183], v[58:61]
	v_mfma_f32_16x16x32_bf16 v[54:57], v[142:145], v[204:207], v[54:57]
	v_mfma_f32_16x16x32_bf16 v[50:53], v[150:153], v[204:207], v[50:53]
	v_mfma_f32_16x16x32_bf16 v[38:41], v[142:145], v[212:215], v[38:41]
	v_mfma_f32_16x16x32_bf16 v[34:37], v[150:153], v[212:215], v[34:37]
	v_mfma_f32_16x16x32_bf16 v[22:25], v[142:145], v[220:223], v[22:25]
	v_mfma_f32_16x16x32_bf16 v[18:21], v[150:153], v[220:223], v[18:21]
	s_setprio 0
	s_setprio 1
	v_mfma_f32_16x16x32_bf16 v[46:49], v[154:157], v[176:179], v[46:49]
	v_mfma_f32_16x16x32_bf16 v[42:45], v[162:165], v[176:179], v[42:45]
	v_mfma_f32_16x16x32_bf16 v[30:33], v[154:157], v[200:203], v[30:33]
	v_mfma_f32_16x16x32_bf16 v[26:29], v[162:165], v[200:203], v[26:29]
	v_mfma_f32_16x16x32_bf16 v[14:17], v[154:157], v[208:211], v[14:17]
	v_mfma_f32_16x16x32_bf16 v[10:13], v[162:165], v[208:211], v[10:13]
	v_mfma_f32_16x16x32_bf16 v[6:9], v[154:157], v[216:219], v[6:9]
	v_mfma_f32_16x16x32_bf16 v[2:5], v[162:165], v[216:219], v[2:5]
	v_mfma_f32_16x16x32_bf16 v[46:49], v[158:161], v[180:183], v[46:49]
	v_mfma_f32_16x16x32_bf16 v[42:45], v[172:175], v[180:183], v[42:45]
	v_mfma_f32_16x16x32_bf16 v[30:33], v[158:161], v[204:207], v[30:33]
	v_mfma_f32_16x16x32_bf16 v[26:29], v[172:175], v[204:207], v[26:29]
	v_mfma_f32_16x16x32_bf16 v[14:17], v[158:161], v[212:215], v[14:17]
	v_mfma_f32_16x16x32_bf16 v[10:13], v[172:175], v[212:215], v[10:13]
	v_mfma_f32_16x16x32_bf16 v[6:9], v[158:161], v[220:223], v[6:9]
	v_mfma_f32_16x16x32_bf16 v[2:5], v[172:175], v[220:223], v[2:5]
	s_setprio 0
	s_barrier
	s_add_i32 s42, s42, 2
	s_add_u32 s40, s40, 0x100
	s_addc_u32 s41, s41, 0
	s_add_u32 s18, s18, 0x100
	s_addc_u32 s19, s19, 0
	s_cmp_gt_u32 s42, 13
	s_cbranch_scc0 .LBB0_557
	s_and_b64 vcc, exec, s[10:11]
	s_cbranch_vccz .LBB0_560
	s_barrier

.LBB0_783:
	s_mov_b32 s100, 0xc0c00000
	v_mov_b32_e32 v203, 0x41000000
	s_add_i32 s2, 0, 0x20000
	s_nop 15
	s_nop 15
	v_add_u32_e32 v2, s2, v178
	ds_read_b128 v[10:13], v2
	v_readlane_b32 s3, v238, 9
	v_add_u32_e32 v18, s47, v175
	v_ashrrev_i32_e32 v19, 31, v18
	v_add_u32_e32 v6, s3, v179
	ds_read_b128 v[6:9], v6
	s_waitcnt lgkmcnt(0)
	v_pk_add_f32 v[24:25], v[158:159], v[10:11]
	v_pk_add_f32 v[22:23], v[160:161], v[12:13]
	v_min_f32_e32 v25, 0x40e00000, v25
	v_min_f32_e32 v24, 0x40e00000, v24
	v_mul_f32_e32 v30, 0xc01d265f, v24
	v_mul_f32_e32 v31, 0xc01d265f, v25
	v_min_f32_e32 v23, 0x40e00000, v23
	v_min_f32_e32 v22, 0x40e00000, v22
	v_exp_f32_e32 v30, v30
	v_exp_f32_e32 v31, v31
	v_add_u32_e32 v2, s3, v178
	v_mul_f32_e32 v32, 0xc01d265f, v22
	v_mul_f32_e32 v33, 0xc01d265f, v23
	ds_read_b128 v[14:17], v2
	v_exp_f32_e32 v32, v32
	v_exp_f32_e32 v33, v33
	v_pk_add_f32 v[30:31], v[30:31], 1.0 op_sel_hi:[1,0]
	v_add_u32_e32 v2, s2, v179
	v_rcp_f32_e32 v30, v30
	v_rcp_f32_e32 v31, v31
	v_pk_add_f32 v[32:33], v[32:33], 1.0 op_sel_hi:[1,0]
	s_waitcnt lgkmcnt(0)
	v_pk_add_f32 v[14:15], v[14:15], 1.0 op_sel_hi:[1,0]
	v_pk_add_f32 v[16:17], v[16:17], 1.0 op_sel_hi:[1,0]
	v_pk_add_f32 v[28:29], v[154:155], v[14:15]
	v_rcp_f32_e32 v32, v32
	v_rcp_f32_e32 v33, v33
	ds_read_b128 v[2:5], v2
	v_med3_f32 v28, v28, s100, v203
	v_pk_add_f32 v[26:27], v[156:157], v[16:17]
	v_med3_f32 v29, v29, s100, v203
	v_pk_mul_f32 v[24:25], v[24:25], v[30:31]
	v_med3_f32 v26, v26, s100, v203
	v_mul_f32_e32 v154, v28, v24
	v_med3_f32 v27, v27, s100, v203
	v_pk_mul_f32 v[22:23], v[22:23], v[32:33]
	v_mul_f32_e32 v155, v29, v25
	v_mul_f32_e32 v156, v26, v22
	v_mul_f32_e32 v157, v27, v23
	s_waitcnt lgkmcnt(0)
	v_pk_add_f32 v[22:23], v[152:153], v[4:5]
	v_pk_add_f32 v[24:25], v[150:151], v[2:3]
	v_min_f32_e32 v23, 0x40e00000, v23
	v_min_f32_e32 v22, 0x40e00000, v22
	v_min_f32_e32 v25, 0x40e00000, v25
	v_min_f32_e32 v24, 0x40e00000, v24
	v_mul_f32_e32 v30, 0xc01d265f, v24
	v_mul_f32_e32 v31, 0xc01d265f, v25
	v_mul_f32_e32 v32, 0xc01d265f, v22
	v_mul_f32_e32 v33, 0xc01d265f, v23
	v_exp_f32_e32 v30, v30
	v_exp_f32_e32 v31, v31
	v_exp_f32_e32 v32, v32
	v_exp_f32_e32 v33, v33
	v_pk_add_f32 v[6:7], v[6:7], 1.0 op_sel_hi:[1,0]
	v_pk_add_f32 v[8:9], v[8:9], 1.0 op_sel_hi:[1,0]
	v_pk_add_f32 v[26:27], v[148:149], v[8:9]
	v_pk_add_f32 v[30:31], v[30:31], 1.0 op_sel_hi:[1,0]
	v_pk_add_f32 v[28:29], v[146:147], v[6:7]
	v_pk_add_f32 v[32:33], v[32:33], 1.0 op_sel_hi:[1,0]
	v_rcp_f32_e32 v30, v30
	v_rcp_f32_e32 v31, v31
	v_rcp_f32_e32 v32, v32
	v_rcp_f32_e32 v33, v33
	v_med3_f32 v26, v26, s100, v203
	v_med3_f32 v28, v28, s100, v203
	v_med3_f32 v27, v27, s100, v203
	v_med3_f32 v29, v29, s100, v203
	v_pk_mul_f32 v[22:23], v[22:23], v[32:33]
	v_pk_mul_f32 v[24:25], v[24:25], v[30:31]
	v_mul_f32_e32 v24, v28, v24
	v_mul_f32_e32 v26, v26, v22
	v_mul_f32_e32 v25, v29, v25
	v_mul_f32_e32 v27, v27, v23
	v_cvt_pk_fp8_f32 v22, v154, v155
	v_cvt_pk_fp8_f32 v23, v24, v25
	v_add_u32_e32 v20, s48, v180
	v_lshlrev_b64 v[18:19], 10, v[18:19]
	v_cvt_pk_fp8_f32 v22, v156, v157 op_sel:[0,0,1]
	v_cvt_pk_fp8_f32 v23, v26, v27 op_sel:[0,0,1]
	v_ashrrev_i32_e32 v21, 31, v20
	v_lshl_add_u64 v[18:19], s[6:7], 0, v[18:19]
	v_lshl_add_u64 v[18:19], v[18:19], 0, v[20:21]
	flat_store_dwordx2 v[18:19], v[22:23]
	v_pk_add_f32 v[22:23], v[142:143], v[10:11]
	v_pk_add_f32 v[20:21], v[144:145], v[12:13]
	v_min_f32_e32 v23, 0x40e00000, v23
	v_min_f32_e32 v22, 0x40e00000, v22
	v_mul_f32_e32 v28, 0xc01d265f, v22
	v_mul_f32_e32 v29, 0xc01d265f, v23
	v_min_f32_e32 v21, 0x40e00000, v21
	v_min_f32_e32 v20, 0x40e00000, v20
	v_exp_f32_e32 v28, v28
	v_exp_f32_e32 v29, v29
	v_mul_f32_e32 v30, 0xc01d265f, v20
	v_mul_f32_e32 v31, 0xc01d265f, v21
	v_exp_f32_e32 v30, v30
	v_exp_f32_e32 v31, v31
	v_pk_add_f32 v[28:29], v[28:29], 1.0 op_sel_hi:[1,0]
	v_pk_add_f32 v[26:27], v[138:139], v[14:15]
	v_rcp_f32_e32 v28, v28
	v_rcp_f32_e32 v29, v29
	v_pk_add_f32 v[30:31], v[30:31], 1.0 op_sel_hi:[1,0]
	v_med3_f32 v26, v26, s100, v203
	v_rcp_f32_e32 v30, v30
	v_rcp_f32_e32 v31, v31
	v_pk_add_f32 v[24:25], v[140:141], v[16:17]
	v_med3_f32 v27, v27, s100, v203
	v_pk_mul_f32 v[22:23], v[22:23], v[28:29]
	v_med3_f32 v24, v24, s100, v203
	v_mul_f32_e32 v32, v26, v22
	v_med3_f32 v25, v25, s100, v203
	v_pk_mul_f32 v[20:21], v[20:21], v[30:31]
	v_mul_f32_e32 v33, v27, v23
	v_mul_f32_e32 v138, v24, v20
	v_mul_f32_e32 v139, v25, v21
	v_pk_add_f32 v[20:21], v[136:137], v[4:5]
	v_pk_add_f32 v[22:23], v[134:135], v[2:3]
	v_min_f32_e32 v21, 0x40e00000, v21
	v_min_f32_e32 v20, 0x40e00000, v20
	v_min_f32_e32 v23, 0x40e00000, v23
	v_min_f32_e32 v22, 0x40e00000, v22
	v_mul_f32_e32 v28, 0xc01d265f, v22
	v_mul_f32_e32 v29, 0xc01d265f, v23
	v_mul_f32_e32 v30, 0xc01d265f, v20
	v_mul_f32_e32 v31, 0xc01d265f, v21
	v_exp_f32_e32 v28, v28
	v_exp_f32_e32 v29, v29
	v_exp_f32_e32 v30, v30
	v_exp_f32_e32 v31, v31
	v_pk_add_f32 v[24:25], v[132:133], v[8:9]
	v_pk_add_f32 v[28:29], v[28:29], 1.0 op_sel_hi:[1,0]
	v_pk_add_f32 v[26:27], v[130:131], v[6:7]
	v_pk_add_f32 v[30:31], v[30:31], 1.0 op_sel_hi:[1,0]
	v_rcp_f32_e32 v28, v28
	v_rcp_f32_e32 v29, v29
	v_rcp_f32_e32 v30, v30
	v_rcp_f32_e32 v31, v31
	v_med3_f32 v24, v24, s100, v203
	v_med3_f32 v26, v26, s100, v203
	v_med3_f32 v25, v25, s100, v203
	v_med3_f32 v27, v27, s100, v203
	v_pk_mul_f32 v[20:21], v[20:21], v[30:31]
	v_pk_mul_f32 v[22:23], v[22:23], v[28:29]
	v_mul_f32_e32 v22, v26, v22
	v_mul_f32_e32 v24, v24, v20
	v_mul_f32_e32 v23, v27, v23
	v_mul_f32_e32 v25, v25, v21
	v_cvt_pk_fp8_f32 v20, v32, v33
	v_cvt_pk_fp8_f32 v21, v22, v23
	v_add_co_u32_e32 v22, vcc, s69, v18
	v_cvt_pk_fp8_f32 v20, v138, v139 op_sel:[0,0,1]
	v_cvt_pk_fp8_f32 v21, v24, v25 op_sel:[0,0,1]
	v_addc_co_u32_e32 v23, vcc, 0, v19, vcc
	v_pk_add_f32 v[26:27], v[122:123], v[14:15]
	flat_store_dwordx2 v[22:23], v[20:21]
	v_pk_add_f32 v[22:23], v[126:127], v[10:11]
	v_pk_add_f32 v[20:21], v[128:129], v[12:13]
	v_min_f32_e32 v23, 0x40e00000, v23
	v_min_f32_e32 v22, 0x40e00000, v22
	v_mul_f32_e32 v28, 0xc01d265f, v22
	v_mul_f32_e32 v29, 0xc01d265f, v23
	v_min_f32_e32 v21, 0x40e00000, v21
	v_min_f32_e32 v20, 0x40e00000, v20
	v_exp_f32_e32 v28, v28
	v_exp_f32_e32 v29, v29
	v_mul_f32_e32 v30, 0xc01d265f, v20
	v_mul_f32_e32 v31, 0xc01d265f, v21
	v_exp_f32_e32 v30, v30
	v_exp_f32_e32 v31, v31
	v_pk_add_f32 v[28:29], v[28:29], 1.0 op_sel_hi:[1,0]
	v_med3_f32 v26, v26, s100, v203
	v_rcp_f32_e32 v28, v28
	v_rcp_f32_e32 v29, v29
	v_pk_add_f32 v[30:31], v[30:31], 1.0 op_sel_hi:[1,0]
	v_pk_add_f32 v[24:25], v[124:125], v[16:17]
	v_rcp_f32_e32 v30, v30
	v_rcp_f32_e32 v31, v31
	v_med3_f32 v27, v27, s100, v203
	v_pk_mul_f32 v[22:23], v[22:23], v[28:29]
	v_med3_f32 v24, v24, s100, v203
	v_mul_f32_e32 v32, v26, v22
	v_med3_f32 v25, v25, s100, v203
	v_pk_mul_f32 v[20:21], v[20:21], v[30:31]
	v_mul_f32_e32 v33, v27, v23
	v_mul_f32_e32 v122, v24, v20
	v_mul_f32_e32 v123, v25, v21
	v_pk_add_f32 v[20:21], v[120:121], v[4:5]
	v_pk_add_f32 v[22:23], v[118:119], v[2:3]
	v_min_f32_e32 v21, 0x40e00000, v21
	v_min_f32_e32 v20, 0x40e00000, v20
	v_min_f32_e32 v23, 0x40e00000, v23
	v_min_f32_e32 v22, 0x40e00000, v22
	v_mul_f32_e32 v28, 0xc01d265f, v22
	v_mul_f32_e32 v29, 0xc01d265f, v23
	v_mul_f32_e32 v30, 0xc01d265f, v20
	v_mul_f32_e32 v31, 0xc01d265f, v21
	v_exp_f32_e32 v28, v28
	v_exp_f32_e32 v29, v29
	v_exp_f32_e32 v30, v30
	v_exp_f32_e32 v31, v31
	v_pk_add_f32 v[24:25], v[116:117], v[8:9]
	v_pk_add_f32 v[28:29], v[28:29], 1.0 op_sel_hi:[1,0]
	v_pk_add_f32 v[26:27], v[114:115], v[6:7]
	v_pk_add_f32 v[30:31], v[30:31], 1.0 op_sel_hi:[1,0]
	v_rcp_f32_e32 v28, v28
	v_rcp_f32_e32 v29, v29
	v_rcp_f32_e32 v30, v30
	v_rcp_f32_e32 v31, v31
	v_med3_f32 v24, v24, s100, v203
	v_med3_f32 v26, v26, s100, v203
	v_med3_f32 v25, v25, s100, v203
	v_med3_f32 v27, v27, s100, v203
	v_pk_mul_f32 v[20:21], v[20:21], v[30:31]
	v_pk_mul_f32 v[22:23], v[22:23], v[28:29]
	v_mul_f32_e32 v22, v26, v22
	v_mul_f32_e32 v24, v24, v20
	v_mul_f32_e32 v23, v27, v23
	v_mul_f32_e32 v25, v25, v21
	v_cvt_pk_fp8_f32 v20, v32, v33
	v_cvt_pk_fp8_f32 v21, v22, v23
	v_add_co_u32_e32 v22, vcc, s67, v18
	v_cvt_pk_fp8_f32 v20, v122, v123 op_sel:[0,0,1]
	v_cvt_pk_fp8_f32 v21, v24, v25 op_sel:[0,0,1]
	v_addc_co_u32_e32 v23, vcc, 0, v19, vcc
	v_pk_add_f32 v[26:27], v[106:107], v[14:15]
	flat_store_dwordx2 v[22:23], v[20:21]
	v_pk_add_f32 v[22:23], v[110:111], v[10:11]
	v_pk_add_f32 v[20:21], v[112:113], v[12:13]
	v_min_f32_e32 v23, 0x40e00000, v23
	v_min_f32_e32 v22, 0x40e00000, v22
	v_mul_f32_e32 v28, 0xc01d265f, v22
	v_mul_f32_e32 v29, 0xc01d265f, v23
	v_min_f32_e32 v21, 0x40e00000, v21
	v_min_f32_e32 v20, 0x40e00000, v20
	v_exp_f32_e32 v28, v28
	v_exp_f32_e32 v29, v29
	v_mul_f32_e32 v30, 0xc01d265f, v20
	v_mul_f32_e32 v31, 0xc01d265f, v21
	v_exp_f32_e32 v30, v30
	v_exp_f32_e32 v31, v31
	v_pk_add_f32 v[28:29], v[28:29], 1.0 op_sel_hi:[1,0]
	v_med3_f32 v26, v26, s100, v203
	v_rcp_f32_e32 v28, v28
	v_rcp_f32_e32 v29, v29
	v_pk_add_f32 v[30:31], v[30:31], 1.0 op_sel_hi:[1,0]
	v_pk_add_f32 v[24:25], v[108:109], v[16:17]
	v_rcp_f32_e32 v30, v30
	v_rcp_f32_e32 v31, v31
	v_med3_f32 v27, v27, s100, v203
	v_pk_mul_f32 v[22:23], v[22:23], v[28:29]
	v_med3_f32 v24, v24, s100, v203
	v_mul_f32_e32 v32, v26, v22
	v_med3_f32 v25, v25, s100, v203
	v_pk_mul_f32 v[20:21], v[20:21], v[30:31]
	v_mul_f32_e32 v33, v27, v23
	v_mul_f32_e32 v106, v24, v20
	v_mul_f32_e32 v107, v25, v21
	v_pk_add_f32 v[20:21], v[104:105], v[4:5]
	v_pk_add_f32 v[22:23], v[102:103], v[2:3]
	v_min_f32_e32 v21, 0x40e00000, v21
	v_min_f32_e32 v20, 0x40e00000, v20
	v_min_f32_e32 v23, 0x40e00000, v23
	v_min_f32_e32 v22, 0x40e00000, v22
	v_mul_f32_e32 v28, 0xc01d265f, v22
	v_mul_f32_e32 v29, 0xc01d265f, v23
	v_mul_f32_e32 v30, 0xc01d265f, v20
	v_mul_f32_e32 v31, 0xc01d265f, v21
	v_exp_f32_e32 v28, v28
	v_exp_f32_e32 v29, v29
	v_exp_f32_e32 v30, v30
	v_exp_f32_e32 v31, v31
	v_pk_add_f32 v[24:25], v[100:101], v[8:9]
	v_pk_add_f32 v[28:29], v[28:29], 1.0 op_sel_hi:[1,0]
	v_pk_add_f32 v[26:27], v[98:99], v[6:7]
	v_pk_add_f32 v[30:31], v[30:31], 1.0 op_sel_hi:[1,0]
	v_rcp_f32_e32 v28, v28
	v_rcp_f32_e32 v29, v29
	v_rcp_f32_e32 v30, v30
	v_rcp_f32_e32 v31, v31
	v_med3_f32 v24, v24, s100, v203
	v_med3_f32 v26, v26, s100, v203
	v_med3_f32 v25, v25, s100, v203
	v_med3_f32 v27, v27, s100, v203
	v_pk_mul_f32 v[20:21], v[20:21], v[30:31]
	v_pk_mul_f32 v[22:23], v[22:23], v[28:29]
	v_mul_f32_e32 v22, v26, v22
	v_mul_f32_e32 v24, v24, v20
	v_mul_f32_e32 v23, v27, v23
	v_mul_f32_e32 v25, v25, v21
	v_cvt_pk_fp8_f32 v20, v32, v33
	v_cvt_pk_fp8_f32 v21, v22, v23
	s_mov_b32 s2, 0xc000
	v_add_co_u32_e32 v22, vcc, s2, v18
	v_cvt_pk_fp8_f32 v20, v106, v107 op_sel:[0,0,1]
	v_cvt_pk_fp8_f32 v21, v24, v25 op_sel:[0,0,1]
	v_addc_co_u32_e32 v23, vcc, 0, v19, vcc
	v_pk_add_f32 v[26:27], v[90:91], v[14:15]
	flat_store_dwordx2 v[22:23], v[20:21]
	v_pk_add_f32 v[22:23], v[94:95], v[10:11]
	v_pk_add_f32 v[20:21], v[96:97], v[12:13]
	v_min_f32_e32 v23, 0x40e00000, v23
	v_min_f32_e32 v22, 0x40e00000, v22
	v_mul_f32_e32 v28, 0xc01d265f, v22
	v_mul_f32_e32 v29, 0xc01d265f, v23
	v_min_f32_e32 v21, 0x40e00000, v21
	v_min_f32_e32 v20, 0x40e00000, v20
	v_exp_f32_e32 v28, v28
	v_exp_f32_e32 v29, v29
	v_mul_f32_e32 v30, 0xc01d265f, v20
	v_mul_f32_e32 v31, 0xc01d265f, v21
	v_exp_f32_e32 v30, v30
	v_exp_f32_e32 v31, v31
	v_pk_add_f32 v[28:29], v[28:29], 1.0 op_sel_hi:[1,0]
	v_med3_f32 v26, v26, s100, v203
	v_rcp_f32_e32 v28, v28
	v_rcp_f32_e32 v29, v29
	v_pk_add_f32 v[30:31], v[30:31], 1.0 op_sel_hi:[1,0]
	v_pk_add_f32 v[24:25], v[92:93], v[16:17]
	v_rcp_f32_e32 v30, v30
	v_rcp_f32_e32 v31, v31
	v_med3_f32 v27, v27, s100, v203
	v_pk_mul_f32 v[22:23], v[22:23], v[28:29]
	v_med3_f32 v24, v24, s100, v203
	v_mul_f32_e32 v32, v26, v22
	v_med3_f32 v25, v25, s100, v203
	v_pk_mul_f32 v[20:21], v[20:21], v[30:31]
	v_mul_f32_e32 v33, v27, v23
	v_mul_f32_e32 v90, v24, v20
	v_mul_f32_e32 v91, v25, v21
	v_pk_add_f32 v[20:21], v[88:89], v[4:5]
	v_pk_add_f32 v[22:23], v[86:87], v[2:3]
	v_min_f32_e32 v21, 0x40e00000, v21
	v_min_f32_e32 v20, 0x40e00000, v20
	v_min_f32_e32 v23, 0x40e00000, v23
	v_min_f32_e32 v22, 0x40e00000, v22
	v_mul_f32_e32 v28, 0xc01d265f, v22
	v_mul_f32_e32 v29, 0xc01d265f, v23
	v_mul_f32_e32 v30, 0xc01d265f, v20
	v_mul_f32_e32 v31, 0xc01d265f, v21
	v_exp_f32_e32 v28, v28
	v_exp_f32_e32 v29, v29
	v_exp_f32_e32 v30, v30
	v_exp_f32_e32 v31, v31
	v_pk_add_f32 v[24:25], v[84:85], v[8:9]
	v_pk_add_f32 v[28:29], v[28:29], 1.0 op_sel_hi:[1,0]
	v_pk_add_f32 v[26:27], v[82:83], v[6:7]
	v_pk_add_f32 v[30:31], v[30:31], 1.0 op_sel_hi:[1,0]
	v_rcp_f32_e32 v28, v28
	v_rcp_f32_e32 v29, v29
	v_rcp_f32_e32 v30, v30
	v_rcp_f32_e32 v31, v31
	v_med3_f32 v24, v24, s100, v203
	v_med3_f32 v26, v26, s100, v203
	v_med3_f32 v25, v25, s100, v203
	v_med3_f32 v27, v27, s100, v203
	v_pk_mul_f32 v[20:21], v[20:21], v[30:31]
	v_pk_mul_f32 v[22:23], v[22:23], v[28:29]
	v_mul_f32_e32 v22, v26, v22
	v_mul_f32_e32 v24, v24, v20
	v_mul_f32_e32 v23, v27, v23
	v_mul_f32_e32 v25, v25, v21
	v_cvt_pk_fp8_f32 v20, v32, v33
	v_cvt_pk_fp8_f32 v21, v22, v23
	s_mov_b32 s2, 0x20000
	v_add_co_u32_e32 v22, vcc, s2, v18
	v_cvt_pk_fp8_f32 v20, v90, v91 op_sel:[0,0,1]
	v_cvt_pk_fp8_f32 v21, v24, v25 op_sel:[0,0,1]
	v_addc_co_u32_e32 v23, vcc, 0, v19, vcc
	v_pk_add_f32 v[26:27], v[74:75], v[14:15]
	flat_store_dwordx2 v[22:23], v[20:21]
	v_pk_add_f32 v[22:23], v[78:79], v[10:11]
	v_pk_add_f32 v[20:21], v[80:81], v[12:13]
	v_min_f32_e32 v23, 0x40e00000, v23
	v_min_f32_e32 v22, 0x40e00000, v22
	v_mul_f32_e32 v28, 0xc01d265f, v22
	v_mul_f32_e32 v29, 0xc01d265f, v23
	v_min_f32_e32 v21, 0x40e00000, v21
	v_min_f32_e32 v20, 0x40e00000, v20
	v_exp_f32_e32 v28, v28
	v_exp_f32_e32 v29, v29
	v_mul_f32_e32 v30, 0xc01d265f, v20
	v_mul_f32_e32 v31, 0xc01d265f, v21
	v_exp_f32_e32 v30, v30
	v_exp_f32_e32 v31, v31
	v_pk_add_f32 v[28:29], v[28:29], 1.0 op_sel_hi:[1,0]
	v_med3_f32 v26, v26, s100, v203
	v_rcp_f32_e32 v28, v28
	v_rcp_f32_e32 v29, v29
	v_pk_add_f32 v[30:31], v[30:31], 1.0 op_sel_hi:[1,0]
	v_pk_add_f32 v[24:25], v[76:77], v[16:17]
	v_rcp_f32_e32 v30, v30
	v_rcp_f32_e32 v31, v31
	v_med3_f32 v27, v27, s100, v203
	v_pk_mul_f32 v[22:23], v[22:23], v[28:29]
	v_med3_f32 v24, v24, s100, v203
	v_mul_f32_e32 v32, v26, v22
	v_med3_f32 v25, v25, s100, v203
	v_pk_mul_f32 v[20:21], v[20:21], v[30:31]
	v_mul_f32_e32 v33, v27, v23
	v_mul_f32_e32 v74, v24, v20
	v_mul_f32_e32 v75, v25, v21
	v_pk_add_f32 v[20:21], v[72:73], v[4:5]
	v_pk_add_f32 v[22:23], v[70:71], v[2:3]
	v_min_f32_e32 v21, 0x40e00000, v21
	v_min_f32_e32 v20, 0x40e00000, v20
	v_min_f32_e32 v23, 0x40e00000, v23
	v_min_f32_e32 v22, 0x40e00000, v22
	v_mul_f32_e32 v28, 0xc01d265f, v22
	v_mul_f32_e32 v29, 0xc01d265f, v23
	v_mul_f32_e32 v30, 0xc01d265f, v20
	v_mul_f32_e32 v31, 0xc01d265f, v21
	v_exp_f32_e32 v28, v28
	v_exp_f32_e32 v29, v29
	v_exp_f32_e32 v30, v30
	v_exp_f32_e32 v31, v31
	v_pk_add_f32 v[24:25], v[68:69], v[8:9]
	v_pk_add_f32 v[28:29], v[28:29], 1.0 op_sel_hi:[1,0]
	v_pk_add_f32 v[26:27], v[66:67], v[6:7]
	v_pk_add_f32 v[30:31], v[30:31], 1.0 op_sel_hi:[1,0]
	v_rcp_f32_e32 v28, v28
	v_rcp_f32_e32 v29, v29
	v_rcp_f32_e32 v30, v30
	v_rcp_f32_e32 v31, v31
	v_med3_f32 v24, v24, s100, v203
	v_med3_f32 v26, v26, s100, v203
	v_med3_f32 v25, v25, s100, v203
	v_med3_f32 v27, v27, s100, v203
	v_pk_mul_f32 v[20:21], v[20:21], v[30:31]
	v_pk_mul_f32 v[22:23], v[22:23], v[28:29]
	v_mul_f32_e32 v22, v26, v22
	v_mul_f32_e32 v24, v24, v20
	v_mul_f32_e32 v23, v27, v23
	v_mul_f32_e32 v25, v25, v21
	v_cvt_pk_fp8_f32 v20, v32, v33
	v_cvt_pk_fp8_f32 v21, v22, v23
	s_mov_b32 s2, 0x24000
	v_add_co_u32_e32 v22, vcc, s2, v18
	v_cvt_pk_fp8_f32 v20, v74, v75 op_sel:[0,0,1]
	v_cvt_pk_fp8_f32 v21, v24, v25 op_sel:[0,0,1]
	v_addc_co_u32_e32 v23, vcc, 0, v19, vcc
	v_pk_add_f32 v[26:27], v[58:59], v[14:15]
	flat_store_dwordx2 v[22:23], v[20:21]
	v_pk_add_f32 v[22:23], v[62:63], v[10:11]
	v_pk_add_f32 v[20:21], v[64:65], v[12:13]
	v_min_f32_e32 v23, 0x40e00000, v23
	v_min_f32_e32 v22, 0x40e00000, v22
	v_mul_f32_e32 v28, 0xc01d265f, v22
	v_mul_f32_e32 v29, 0xc01d265f, v23
	v_min_f32_e32 v21, 0x40e00000, v21
	v_min_f32_e32 v20, 0x40e00000, v20
	v_exp_f32_e32 v28, v28
	v_exp_f32_e32 v29, v29
	v_mul_f32_e32 v30, 0xc01d265f, v20
	v_mul_f32_e32 v31, 0xc01d265f, v21
	v_exp_f32_e32 v30, v30
	v_exp_f32_e32 v31, v31
	v_pk_add_f32 v[28:29], v[28:29], 1.0 op_sel_hi:[1,0]
	v_med3_f32 v26, v26, s100, v203
	v_rcp_f32_e32 v28, v28
	v_rcp_f32_e32 v29, v29
	v_pk_add_f32 v[30:31], v[30:31], 1.0 op_sel_hi:[1,0]
	v_pk_add_f32 v[24:25], v[60:61], v[16:17]
	v_rcp_f32_e32 v30, v30
	v_rcp_f32_e32 v31, v31
	v_med3_f32 v27, v27, s100, v203
	v_pk_mul_f32 v[22:23], v[22:23], v[28:29]
	v_med3_f32 v24, v24, s100, v203
	v_mul_f32_e32 v32, v26, v22
	v_med3_f32 v25, v25, s100, v203
	v_pk_mul_f32 v[20:21], v[20:21], v[30:31]
	v_mul_f32_e32 v33, v27, v23
	v_mul_f32_e32 v58, v24, v20
	v_mul_f32_e32 v59, v25, v21
	v_pk_add_f32 v[20:21], v[56:57], v[4:5]
	v_pk_add_f32 v[22:23], v[54:55], v[2:3]
	v_min_f32_e32 v21, 0x40e00000, v21
	v_min_f32_e32 v20, 0x40e00000, v20
	v_min_f32_e32 v23, 0x40e00000, v23
	v_min_f32_e32 v22, 0x40e00000, v22
	v_mul_f32_e32 v28, 0xc01d265f, v22
	v_mul_f32_e32 v29, 0xc01d265f, v23
	v_mul_f32_e32 v30, 0xc01d265f, v20
	v_mul_f32_e32 v31, 0xc01d265f, v21
	v_exp_f32_e32 v28, v28
	v_exp_f32_e32 v29, v29
	v_exp_f32_e32 v30, v30
	v_exp_f32_e32 v31, v31
	v_pk_add_f32 v[24:25], v[52:53], v[8:9]
	v_pk_add_f32 v[28:29], v[28:29], 1.0 op_sel_hi:[1,0]
	v_pk_add_f32 v[26:27], v[50:51], v[6:7]
	v_pk_add_f32 v[30:31], v[30:31], 1.0 op_sel_hi:[1,0]
	v_rcp_f32_e32 v28, v28
	v_rcp_f32_e32 v29, v29
	v_rcp_f32_e32 v30, v30
	v_rcp_f32_e32 v31, v31
	v_med3_f32 v24, v24, s100, v203
	v_med3_f32 v26, v26, s100, v203
	v_med3_f32 v25, v25, s100, v203
	v_med3_f32 v27, v27, s100, v203
	v_pk_mul_f32 v[20:21], v[20:21], v[30:31]
	v_pk_mul_f32 v[22:23], v[22:23], v[28:29]
	v_mul_f32_e32 v22, v26, v22
	v_mul_f32_e32 v24, v24, v20
	v_mul_f32_e32 v23, v27, v23
	v_mul_f32_e32 v25, v25, v21
	v_cvt_pk_fp8_f32 v20, v32, v33
	v_cvt_pk_fp8_f32 v21, v22, v23
	s_mov_b32 s2, 0x28000
	v_add_co_u32_e32 v22, vcc, s2, v18
	v_cvt_pk_fp8_f32 v20, v58, v59 op_sel:[0,0,1]
	v_cvt_pk_fp8_f32 v21, v24, v25 op_sel:[0,0,1]
	v_pk_add_f32 v[10:11], v[46:47], v[10:11]
	v_addc_co_u32_e32 v23, vcc, 0, v19, vcc
	v_min_f32_e32 v11, 0x40e00000, v11
	v_min_f32_e32 v10, 0x40e00000, v10
	flat_store_dwordx2 v[22:23], v[20:21]
	v_pk_add_f32 v[12:13], v[48:49], v[12:13]
	v_mul_f32_e32 v20, 0xc01d265f, v10
	v_mul_f32_e32 v21, 0xc01d265f, v11
	v_min_f32_e32 v13, 0x40e00000, v13
	v_min_f32_e32 v12, 0x40e00000, v12
	v_exp_f32_e32 v20, v20
	v_exp_f32_e32 v21, v21
	v_mul_f32_e32 v22, 0xc01d265f, v12
	v_mul_f32_e32 v23, 0xc01d265f, v13
	v_exp_f32_e32 v22, v22
	v_exp_f32_e32 v23, v23
	v_pk_add_f32 v[20:21], v[20:21], 1.0 op_sel_hi:[1,0]
	v_pk_add_f32 v[14:15], v[42:43], v[14:15]
	v_rcp_f32_e32 v20, v20
	v_rcp_f32_e32 v21, v21
	v_pk_add_f32 v[22:23], v[22:23], 1.0 op_sel_hi:[1,0]
	v_med3_f32 v14, v14, s100, v203
	v_rcp_f32_e32 v22, v22
	v_rcp_f32_e32 v23, v23
	v_pk_add_f32 v[16:17], v[44:45], v[16:17]
	v_med3_f32 v15, v15, s100, v203
	v_pk_mul_f32 v[10:11], v[10:11], v[20:21]
	v_med3_f32 v16, v16, s100, v203
	v_mul_f32_e32 v14, v14, v10
	v_med3_f32 v17, v17, s100, v203
	v_pk_mul_f32 v[12:13], v[12:13], v[22:23]
	v_mul_f32_e32 v15, v15, v11
	v_pk_add_f32 v[2:3], v[38:39], v[2:3]
	v_mul_f32_e32 v16, v16, v12
	v_min_f32_e32 v3, 0x40e00000, v3
	v_min_f32_e32 v2, 0x40e00000, v2
	v_mul_f32_e32 v17, v17, v13
	v_pk_add_f32 v[4:5], v[40:41], v[4:5]
	v_mul_f32_e32 v10, 0xc01d265f, v2
	v_mul_f32_e32 v11, 0xc01d265f, v3
	v_min_f32_e32 v5, 0x40e00000, v5
	v_min_f32_e32 v4, 0x40e00000, v4
	v_exp_f32_e32 v10, v10
	v_exp_f32_e32 v11, v11
	v_mul_f32_e32 v12, 0xc01d265f, v4
	v_mul_f32_e32 v13, 0xc01d265f, v5
	v_exp_f32_e32 v12, v12
	v_exp_f32_e32 v13, v13
	v_pk_add_f32 v[10:11], v[10:11], 1.0 op_sel_hi:[1,0]
	v_pk_add_f32 v[6:7], v[34:35], v[6:7]
	v_rcp_f32_e32 v10, v10
	v_rcp_f32_e32 v11, v11
	v_pk_add_f32 v[12:13], v[12:13], 1.0 op_sel_hi:[1,0]
	v_med3_f32 v6, v6, s100, v203
	v_rcp_f32_e32 v12, v12
	v_rcp_f32_e32 v13, v13
	v_pk_add_f32 v[8:9], v[36:37], v[8:9]
	v_med3_f32 v7, v7, s100, v203
	v_pk_mul_f32 v[2:3], v[2:3], v[10:11]
	v_med3_f32 v8, v8, s100, v203
	v_mul_f32_e32 v6, v6, v2
	v_med3_f32 v9, v9, s100, v203
	v_pk_mul_f32 v[4:5], v[4:5], v[12:13]
	v_mul_f32_e32 v7, v7, v3
	v_mul_f32_e32 v4, v8, v4
	v_mul_f32_e32 v5, v9, v5
	v_cvt_pk_fp8_f32 v2, v14, v15
	v_cvt_pk_fp8_f32 v3, v6, v7
	s_mov_b64 s[2:3], -1
	v_cvt_pk_fp8_f32 v2, v16, v17 op_sel:[0,0,1]
	v_cvt_pk_fp8_f32 v3, v4, v5 op_sel:[0,0,1]
	v_add_co_u32_e32 v4, vcc, 0x2c000, v18
	s_nop 1
	v_addc_co_u32_e32 v5, vcc, 0, v19, vcc
	s_andn2_b64 vcc, exec, s[14:15]
	flat_store_dwordx2 v[4:5], v[2:3]
	s_cbranch_vccnz .LBB0_772
	s_andn2_b64 vcc, exec, s[4:5]
	s_cbranch_vccnz .LBB0_771
	s_barrier
	s_branch .LBB0_771

.LBB0_876:
	s_add_i32 s11, 0, 0x20400
	s_nop 15
	s_nop 15
	v_add_u32_e32 v18, s11, v182
	s_add_i32 s19, 0, 0x20800
	ds_read_b128 v[14:17], v203
	ds_read_b128 v[10:13], v203 offset:16
	ds_read_b128 v[6:9], v203 offset:512
	ds_read_b128 v[2:5], v203 offset:528
	v_add_u32_e32 v19, s19, v182
	v_add_u32_e32 v20, s11, v183
	v_add_u32_e32 v21, s19, v183
	v_add_u32_e32 v22, s11, v184
	v_add_u32_e32 v23, s19, v184
	ds_read_b32 v33, v18
	ds_read_b32 v32, v19
	ds_read_b32 v31, v20
	ds_read_b32 v30, v21
	ds_read_b32 v29, v22
	ds_read_b32 v28, v23
	v_add_u32_e32 v18, s11, v181
	v_add_u32_e32 v20, s19, v181
	ds_read2_b32 v[24:25], v18 offset0:128 offset1:144
	ds_read2_b32 v[26:27], v20 offset0:128 offset1:144
	ds_read2_b32 v[18:19], v18 offset0:160 offset1:176
	ds_read2_b32 v[22:23], v20 offset0:160 offset1:176
	v_add_u32_e32 v20, s18, v185
	v_add_u32_e32 v162, s54, v177
	v_ashrrev_i32_e32 v21, 31, v20
	v_cmp_gt_i32_e32 vcc, s39, v162
	s_and_saveexec_b64 s[18:19], vcc
	s_cbranch_execz .LBB0_878
	v_add_u32_e32 v163, 0, v181
	v_add_u32_e32 v164, 0x20800, v163
	v_add_u32_e32 v163, 0x20400, v163
	ds_read_b32 v166, v164
	ds_read_b32 v165, v163
	s_waitcnt lgkmcnt(0)
	v_pk_add_f32 v[154:155], v[154:155], v[10:11]
	v_pk_add_f32 v[158:159], v[158:159], v[14:15]
	v_mul_f32_e32 v166, 0x41800000, v166
	v_pk_mul_f32 v[154:155], v[154:155], v[166:167] op_sel_hi:[1,0]
	v_pk_mul_f32 v[158:159], v[158:159], v[166:167] op_sel_hi:[1,0]
	v_cvt_pk_fp8_f32 v205, v154, v155
	v_pk_add_f32 v[154:155], v[156:157], v[12:13]
	v_pk_mul_f32 v[154:155], v[154:155], v[166:167] op_sel_hi:[1,0]
	v_pk_add_f32 v[150:151], v[150:151], v[6:7]
	v_pk_add_f32 v[146:147], v[146:147], v[2:3]
	v_cvt_pk_fp8_f32 v204, v158, v159
	v_cvt_pk_fp8_f32 v205, v154, v155 op_sel:[0,0,1]
	v_pk_mul_f32 v[150:151], v[150:151], v[166:167] op_sel_hi:[1,0]
	v_pk_mul_f32 v[146:147], v[146:147], v[166:167] op_sel_hi:[1,0]
	v_cvt_pk_fp8_f32 v154, v150, v151
	v_cvt_pk_fp8_f32 v155, v146, v147
	v_pk_add_f32 v[160:161], v[160:161], v[16:17]
	v_pk_add_f32 v[152:153], v[152:153], v[8:9]
	v_pk_mul_f32 v[160:161], v[160:161], v[166:167] op_sel_hi:[1,0]
	v_pk_add_f32 v[146:147], v[148:149], v[4:5]
	v_mov_b32_e32 v164, v167
	v_cvt_pk_fp8_f32 v204, v160, v161 op_sel:[0,0,1]
	v_pk_mul_f32 v[152:153], v[152:153], v[166:167] op_sel_hi:[1,0]
	v_pk_mul_f32 v[146:147], v[146:147], v[166:167] op_sel_hi:[1,0]
	v_ashrrev_i64 v[164:165], 22, v[164:165]
	v_cvt_pk_fp8_f32 v154, v152, v153 op_sel:[0,0,1]
	v_cvt_pk_fp8_f32 v155, v146, v147 op_sel:[0,0,1]
	v_lshl_add_u64 v[146:147], s[2:3], 0, v[164:165]
	v_lshl_add_u64 v[146:147], v[146:147], 0, v[20:21]
	flat_store_dwordx2 v[146:147], v[204:205]
	flat_store_dwordx2 v[146:147], v[154:155] offset:128
.LBB0_878:
	s_or_b64 exec, exec, s[18:19]
	v_add_u32_e32 v146, s54, v199
	v_cmp_gt_i32_e32 vcc, s39, v146
	s_and_saveexec_b64 s[18:19], vcc
	s_cbranch_execz .LBB0_880
	s_waitcnt lgkmcnt(0)
	v_mul_f32_e32 v146, 0x41800000, v32
	v_pk_add_f32 v[138:139], v[138:139], v[10:11]
	v_pk_mul_f32 v[138:139], v[138:139], v[146:147] op_sel_hi:[1,0]
	v_pk_add_f32 v[142:143], v[142:143], v[14:15]
	v_cvt_pk_fp8_f32 v149, v138, v139
	v_pk_add_f32 v[138:139], v[140:141], v[12:13]
	v_pk_mul_f32 v[142:143], v[142:143], v[146:147] op_sel_hi:[1,0]
	v_pk_mul_f32 v[138:139], v[138:139], v[146:147] op_sel_hi:[1,0]
	v_pk_add_f32 v[134:135], v[134:135], v[6:7]
	v_pk_add_f32 v[130:131], v[130:131], v[2:3]
	v_cvt_pk_fp8_f32 v148, v142, v143
	v_cvt_pk_fp8_f32 v149, v138, v139 op_sel:[0,0,1]
	v_pk_mul_f32 v[134:135], v[134:135], v[146:147] op_sel_hi:[1,0]
	v_pk_mul_f32 v[130:131], v[130:131], v[146:147] op_sel_hi:[1,0]
	v_cvt_pk_fp8_f32 v138, v134, v135
	v_cvt_pk_fp8_f32 v139, v130, v131
	v_pk_add_f32 v[144:145], v[144:145], v[16:17]
	v_pk_add_f32 v[136:137], v[136:137], v[8:9]
	v_pk_mul_f32 v[144:145], v[144:145], v[146:147] op_sel_hi:[1,0]
	v_pk_add_f32 v[130:131], v[132:133], v[4:5]
	v_mov_b32_e32 v32, v167
	v_cvt_pk_fp8_f32 v148, v144, v145 op_sel:[0,0,1]
	v_pk_mul_f32 v[136:137], v[136:137], v[146:147] op_sel_hi:[1,0]
	v_pk_mul_f32 v[130:131], v[130:131], v[146:147] op_sel_hi:[1,0]
	v_ashrrev_i64 v[32:33], 22, v[32:33]
	v_cvt_pk_fp8_f32 v138, v136, v137 op_sel:[0,0,1]
	v_cvt_pk_fp8_f32 v139, v130, v131 op_sel:[0,0,1]
	v_lshl_add_u64 v[32:33], s[2:3], 0, v[32:33]
	v_lshl_add_u64 v[32:33], v[32:33], 0, v[20:21]
	flat_store_dwordx2 v[32:33], v[148:149]
	flat_store_dwordx2 v[32:33], v[138:139] offset:128
.LBB0_880:
	s_or_b64 exec, exec, s[18:19]
	s_waitcnt lgkmcnt(0)
	v_add_u32_e32 v32, s54, v200
	v_cmp_gt_i32_e32 vcc, s39, v32
	s_and_saveexec_b64 s[18:19], vcc
	s_cbranch_execz .LBB0_882
	v_mul_f32_e32 v32, 0x41800000, v30
	v_pk_add_f32 v[122:123], v[122:123], v[10:11]
	v_pk_mul_f32 v[122:123], v[122:123], v[32:33] op_sel_hi:[1,0]
	v_pk_add_f32 v[126:127], v[126:127], v[14:15]
	v_cvt_pk_fp8_f32 v131, v122, v123
	v_pk_add_f32 v[122:123], v[124:125], v[12:13]
	v_pk_mul_f32 v[126:127], v[126:127], v[32:33] op_sel_hi:[1,0]
	v_pk_mul_f32 v[122:123], v[122:123], v[32:33] op_sel_hi:[1,0]
	v_pk_add_f32 v[118:119], v[118:119], v[6:7]
	v_pk_add_f32 v[114:115], v[114:115], v[2:3]
	v_cvt_pk_fp8_f32 v130, v126, v127
	v_cvt_pk_fp8_f32 v131, v122, v123 op_sel:[0,0,1]
	v_pk_mul_f32 v[118:119], v[118:119], v[32:33] op_sel_hi:[1,0]
	v_pk_mul_f32 v[114:115], v[114:115], v[32:33] op_sel_hi:[1,0]
	v_cvt_pk_fp8_f32 v122, v118, v119
	v_cvt_pk_fp8_f32 v123, v114, v115
	v_pk_add_f32 v[128:129], v[128:129], v[16:17]
	v_pk_add_f32 v[120:121], v[120:121], v[8:9]
	v_pk_mul_f32 v[128:129], v[128:129], v[32:33] op_sel_hi:[1,0]
	v_pk_add_f32 v[114:115], v[116:117], v[4:5]
	v_mov_b32_e32 v30, v167
	v_cvt_pk_fp8_f32 v130, v128, v129 op_sel:[0,0,1]
	v_pk_mul_f32 v[120:121], v[120:121], v[32:33] op_sel_hi:[1,0]
	v_pk_mul_f32 v[32:33], v[114:115], v[32:33] op_sel_hi:[1,0]
	v_ashrrev_i64 v[30:31], 22, v[30:31]
	v_cvt_pk_fp8_f32 v122, v120, v121 op_sel:[0,0,1]
	v_cvt_pk_fp8_f32 v123, v32, v33 op_sel:[0,0,1]
	v_lshl_add_u64 v[30:31], s[2:3], 0, v[30:31]
	v_lshl_add_u64 v[30:31], v[30:31], 0, v[20:21]
	flat_store_dwordx2 v[30:31], v[130:131]
	flat_store_dwordx2 v[30:31], v[122:123] offset:128
.LBB0_882:
	s_or_b64 exec, exec, s[18:19]
	v_add_u32_e32 v30, s54, v201
	v_cmp_gt_i32_e32 vcc, s39, v30
	s_and_saveexec_b64 s[18:19], vcc
	s_cbranch_execz .LBB0_884
	v_mul_f32_e32 v30, 0x41800000, v28
	v_pk_add_f32 v[110:111], v[110:111], v[14:15]
	v_pk_add_f32 v[32:33], v[112:113], v[16:17]
	v_pk_mul_f32 v[110:111], v[110:111], v[30:31] op_sel_hi:[1,0]
	v_cvt_pk_fp8_f32 v112, v110, v111
	v_pk_add_f32 v[106:107], v[106:107], v[10:11]
	v_pk_mul_f32 v[32:33], v[32:33], v[30:31] op_sel_hi:[1,0]
	v_pk_mul_f32 v[106:107], v[106:107], v[30:31] op_sel_hi:[1,0]
	v_pk_add_f32 v[102:103], v[102:103], v[6:7]
	v_pk_add_f32 v[98:99], v[98:99], v[2:3]
	v_cvt_pk_fp8_f32 v113, v106, v107
	v_cvt_pk_fp8_f32 v112, v32, v33 op_sel:[0,0,1]
	v_pk_add_f32 v[32:33], v[104:105], v[8:9]
	v_pk_mul_f32 v[102:103], v[102:103], v[30:31] op_sel_hi:[1,0]
	v_pk_mul_f32 v[98:99], v[98:99], v[30:31] op_sel_hi:[1,0]
	v_cvt_pk_fp8_f32 v104, v102, v103
	v_cvt_pk_fp8_f32 v105, v98, v99
	v_pk_add_f32 v[106:107], v[108:109], v[12:13]
	v_pk_add_f32 v[98:99], v[100:101], v[4:5]
	v_pk_mul_f32 v[106:107], v[106:107], v[30:31] op_sel_hi:[1,0]
	v_mov_b32_e32 v28, v167
	v_cvt_pk_fp8_f32 v113, v106, v107 op_sel:[0,0,1]
	v_pk_mul_f32 v[32:33], v[32:33], v[30:31] op_sel_hi:[1,0]
	v_pk_mul_f32 v[30:31], v[98:99], v[30:31] op_sel_hi:[1,0]
	v_ashrrev_i64 v[28:29], 22, v[28:29]
	v_cvt_pk_fp8_f32 v104, v32, v33 op_sel:[0,0,1]
	v_cvt_pk_fp8_f32 v105, v30, v31 op_sel:[0,0,1]
	v_lshl_add_u64 v[28:29], s[2:3], 0, v[28:29]
	v_lshl_add_u64 v[28:29], v[28:29], 0, v[20:21]
	flat_store_dwordx2 v[28:29], v[112:113]
	flat_store_dwordx2 v[28:29], v[104:105] offset:128
.LBB0_884:
	s_or_b64 exec, exec, s[18:19]
	v_add_u32_e32 v28, 0x80, v162
	v_cmp_gt_i32_e32 vcc, s39, v28
	s_and_saveexec_b64 s[18:19], vcc
	s_cbranch_execz .LBB0_886
	v_mul_f32_e32 v26, 0x41800000, v26
	v_pk_add_f32 v[90:91], v[90:91], v[10:11]
	v_pk_add_f32 v[32:33], v[94:95], v[14:15]
	v_pk_mul_f32 v[90:91], v[90:91], v[26:27] op_sel_hi:[1,0]
	v_cvt_pk_fp8_f32 v95, v90, v91
	v_pk_mul_f32 v[32:33], v[32:33], v[26:27] op_sel_hi:[1,0]
	v_cvt_pk_fp8_f32 v94, v32, v33
	v_pk_add_f32 v[32:33], v[92:93], v[12:13]
	v_pk_add_f32 v[82:83], v[82:83], v[2:3]
	v_pk_mul_f32 v[32:33], v[32:33], v[26:27] op_sel_hi:[1,0]
	v_pk_mul_f32 v[82:83], v[82:83], v[26:27] op_sel_hi:[1,0]
	v_cvt_pk_fp8_f32 v95, v32, v33 op_sel:[0,0,1]
	v_pk_add_f32 v[32:33], v[86:87], v[6:7]
	v_pk_mul_f32 v[32:33], v[32:33], v[26:27] op_sel_hi:[1,0]
	v_pk_add_f32 v[30:31], v[96:97], v[16:17]
	v_cvt_pk_fp8_f32 v86, v32, v33
	v_cvt_pk_fp8_f32 v87, v82, v83
	v_pk_mul_f32 v[30:31], v[30:31], v[26:27] op_sel_hi:[1,0]
	v_pk_add_f32 v[32:33], v[84:85], v[4:5]
	v_cvt_pk_fp8_f32 v94, v30, v31 op_sel:[0,0,1]
	v_pk_add_f32 v[30:31], v[88:89], v[8:9]
	v_mov_b32_e32 v28, v167
	v_mov_b32_e32 v29, v24
	v_pk_mul_f32 v[30:31], v[30:31], v[26:27] op_sel_hi:[1,0]
	v_pk_mul_f32 v[32:33], v[32:33], v[26:27] op_sel_hi:[1,0]
	v_ashrrev_i64 v[28:29], 22, v[28:29]
	v_cvt_pk_fp8_f32 v86, v30, v31 op_sel:[0,0,1]
	v_cvt_pk_fp8_f32 v87, v32, v33 op_sel:[0,0,1]
	v_lshl_add_u64 v[28:29], s[2:3], 0, v[28:29]
	v_lshl_add_u64 v[28:29], v[28:29], 0, v[20:21]
	flat_store_dwordx2 v[28:29], v[94:95]
	flat_store_dwordx2 v[28:29], v[86:87] offset:128
.LBB0_886:
	s_or_b64 exec, exec, s[18:19]
	v_add_u32_e32 v24, 0x90, v162
	v_cmp_gt_i32_e32 vcc, s39, v24
	s_and_saveexec_b64 s[18:19], vcc
	s_cbranch_execz .LBB0_888
	v_mul_f32_e32 v26, 0x41800000, v27
	v_pk_add_f32 v[32:33], v[74:75], v[10:11]
	v_pk_mul_f32 v[32:33], v[32:33], v[26:27] op_sel_hi:[1,0]
	v_pk_add_f32 v[30:31], v[78:79], v[14:15]
	v_cvt_pk_fp8_f32 v75, v32, v33
	v_pk_mul_f32 v[30:31], v[30:31], v[26:27] op_sel_hi:[1,0]
	v_cvt_pk_fp8_f32 v74, v30, v31
	v_pk_add_f32 v[30:31], v[76:77], v[12:13]
	v_pk_add_f32 v[32:33], v[66:67], v[2:3]
	v_pk_mul_f32 v[30:31], v[30:31], v[26:27] op_sel_hi:[1,0]
	v_pk_mul_f32 v[32:33], v[32:33], v[26:27] op_sel_hi:[1,0]
	v_cvt_pk_fp8_f32 v75, v30, v31 op_sel:[0,0,1]
	v_pk_add_f32 v[30:31], v[70:71], v[6:7]
	v_pk_mul_f32 v[30:31], v[30:31], v[26:27] op_sel_hi:[1,0]
	v_pk_add_f32 v[28:29], v[80:81], v[16:17]
	v_cvt_pk_fp8_f32 v66, v30, v31
	v_cvt_pk_fp8_f32 v67, v32, v33
	v_pk_mul_f32 v[28:29], v[28:29], v[26:27] op_sel_hi:[1,0]
	v_pk_add_f32 v[30:31], v[68:69], v[4:5]
	v_cvt_pk_fp8_f32 v74, v28, v29 op_sel:[0,0,1]
	v_pk_add_f32 v[28:29], v[72:73], v[8:9]
	v_mov_b32_e32 v24, v167
	v_pk_mul_f32 v[28:29], v[28:29], v[26:27] op_sel_hi:[1,0]
	v_pk_mul_f32 v[26:27], v[30:31], v[26:27] op_sel_hi:[1,0]
	v_ashrrev_i64 v[24:25], 22, v[24:25]
	v_cvt_pk_fp8_f32 v66, v28, v29 op_sel:[0,0,1]
	v_cvt_pk_fp8_f32 v67, v26, v27 op_sel:[0,0,1]
	v_lshl_add_u64 v[24:25], s[2:3], 0, v[24:25]
	v_lshl_add_u64 v[24:25], v[24:25], 0, v[20:21]
	flat_store_dwordx2 v[24:25], v[74:75]
	flat_store_dwordx2 v[24:25], v[66:67] offset:128
.LBB0_888:
	s_or_b64 exec, exec, s[18:19]
	v_add_u32_e32 v24, 0xa0, v162
	v_cmp_gt_i32_e32 vcc, s39, v24
	s_and_saveexec_b64 s[18:19], vcc
	s_cbranch_execz .LBB0_890
	v_mul_f32_e32 v22, 0x41800000, v22
	v_pk_add_f32 v[30:31], v[58:59], v[10:11]
	v_pk_mul_f32 v[30:31], v[30:31], v[22:23] op_sel_hi:[1,0]
	v_pk_add_f32 v[28:29], v[62:63], v[14:15]
	v_cvt_pk_fp8_f32 v33, v30, v31
	v_pk_mul_f32 v[28:29], v[28:29], v[22:23] op_sel_hi:[1,0]
	v_cvt_pk_fp8_f32 v32, v28, v29
	v_pk_add_f32 v[28:29], v[60:61], v[12:13]
	v_pk_add_f32 v[30:31], v[50:51], v[2:3]
	v_pk_mul_f32 v[28:29], v[28:29], v[22:23] op_sel_hi:[1,0]
	v_pk_mul_f32 v[30:31], v[30:31], v[22:23] op_sel_hi:[1,0]
	v_cvt_pk_fp8_f32 v33, v28, v29 op_sel:[0,0,1]
	v_pk_add_f32 v[28:29], v[54:55], v[6:7]
	v_pk_mul_f32 v[28:29], v[28:29], v[22:23] op_sel_hi:[1,0]
	v_pk_add_f32 v[26:27], v[64:65], v[16:17]
	v_cvt_pk_fp8_f32 v50, v28, v29
	v_cvt_pk_fp8_f32 v51, v30, v31
	v_pk_mul_f32 v[26:27], v[26:27], v[22:23] op_sel_hi:[1,0]
	v_pk_add_f32 v[28:29], v[52:53], v[4:5]
	v_cvt_pk_fp8_f32 v32, v26, v27 op_sel:[0,0,1]
	v_pk_add_f32 v[26:27], v[56:57], v[8:9]
	v_mov_b32_e32 v24, v167
	v_mov_b32_e32 v25, v18
	v_pk_mul_f32 v[26:27], v[26:27], v[22:23] op_sel_hi:[1,0]
	v_pk_mul_f32 v[28:29], v[28:29], v[22:23] op_sel_hi:[1,0]
	v_ashrrev_i64 v[24:25], 22, v[24:25]
	v_cvt_pk_fp8_f32 v50, v26, v27 op_sel:[0,0,1]
	v_cvt_pk_fp8_f32 v51, v28, v29 op_sel:[0,0,1]
	v_lshl_add_u64 v[24:25], s[2:3], 0, v[24:25]
	v_lshl_add_u64 v[24:25], v[24:25], 0, v[20:21]
	flat_store_dwordx2 v[24:25], v[32:33]
	flat_store_dwordx2 v[24:25], v[50:51] offset:128
.LBB0_890:
	s_or_b64 exec, exec, s[18:19]
	v_add_u32_e32 v18, 0xb0, v162
	v_cmp_gt_i32_e32 vcc, s39, v18
	s_and_saveexec_b64 s[18:19], vcc
	s_cbranch_execz .LBB0_892
	v_mov_b32_e32 v18, v167
	v_ashrrev_i64 v[18:19], 22, v[18:19]
	v_mul_f32_e32 v22, 0x41800000, v23
	v_lshl_add_u64 v[18:19], s[2:3], 0, v[18:19]
	v_pk_add_f32 v[10:11], v[42:43], v[10:11]
	v_lshl_add_u64 v[18:19], v[18:19], 0, v[20:21]
	v_pk_add_f32 v[14:15], v[46:47], v[14:15]
	v_pk_mul_f32 v[10:11], v[10:11], v[22:23] op_sel_hi:[1,0]
	v_pk_add_f32 v[6:7], v[38:39], v[6:7]
	v_pk_add_f32 v[2:3], v[34:35], v[2:3]
	v_pk_mul_f32 v[14:15], v[14:15], v[22:23] op_sel_hi:[1,0]
	v_cvt_pk_fp8_f32 v21, v10, v11
	v_pk_mul_f32 v[6:7], v[6:7], v[22:23] op_sel_hi:[1,0]
	v_pk_mul_f32 v[2:3], v[2:3], v[22:23] op_sel_hi:[1,0]
	v_cvt_pk_fp8_f32 v20, v14, v15
	v_cvt_pk_fp8_f32 v10, v6, v7
	v_cvt_pk_fp8_f32 v11, v2, v3
	v_pk_add_f32 v[16:17], v[48:49], v[16:17]
	v_pk_add_f32 v[12:13], v[44:45], v[12:13]
	v_pk_add_f32 v[8:9], v[40:41], v[8:9]
	v_pk_add_f32 v[4:5], v[36:37], v[4:5]
	v_pk_mul_f32 v[16:17], v[16:17], v[22:23] op_sel_hi:[1,0]
	v_pk_mul_f32 v[12:13], v[12:13], v[22:23] op_sel_hi:[1,0]
	v_pk_mul_f32 v[8:9], v[8:9], v[22:23] op_sel_hi:[1,0]
	v_pk_mul_f32 v[4:5], v[4:5], v[22:23] op_sel_hi:[1,0]
	v_cvt_pk_fp8_f32 v20, v16, v17 op_sel:[0,0,1]
	v_cvt_pk_fp8_f32 v21, v12, v13 op_sel:[0,0,1]
	v_cvt_pk_fp8_f32 v10, v8, v9 op_sel:[0,0,1]
	v_cvt_pk_fp8_f32 v11, v4, v5 op_sel:[0,0,1]
	flat_store_dwordx2 v[18:19], v[20:21]
	flat_store_dwordx2 v[18:19], v[10:11] offset:128

.LBB0_899:
	ds_write2_b32 v135, v66, v67 offset1:1
	ds_write2_b32 v135, v68, v69 offset0:2 offset1:3
	ds_write2_b32 v139, v70, v71 offset1:1
	ds_write2_b32 v140, v72, v73 offset1:1
	ds_write2_b32 v141, v74, v75 offset1:1
	ds_write2_b32 v142, v76, v77 offset1:1
	ds_write2_b32 v143, v78, v79 offset1:1
	ds_write2_b32 v144, v80, v81 offset1:1
	ds_write2_b32 v145, v82, v83 offset1:1
	ds_write2_b32 v146, v84, v85 offset1:1
	ds_write2_b32 v147, v86, v87 offset1:1
	ds_write2_b32 v148, v88, v89 offset1:1
	ds_write2_b32 v149, v90, v91 offset1:1
	ds_write2_b32 v150, v92, v93 offset1:1
	ds_write2_b32 v151, v94, v95 offset1:1
	ds_write2_b32 v152, v96, v97 offset1:1
	ds_write2_b32 v153, v98, v99 offset1:1
	ds_write2_b32 v154, v100, v101 offset1:1
	ds_write2_b32 v155, v102, v103 offset1:1
	ds_write2_b32 v156, v104, v105 offset1:1
	ds_write2_b32 v157, v106, v107 offset1:1
	ds_write2_b32 v158, v108, v109 offset1:1
	ds_write2_b32 v159, v110, v111 offset1:1
	ds_write2_b32 v160, v112, v113 offset1:1
	ds_write2_b32 v161, v114, v115 offset1:1
	ds_write2_b32 v162, v116, v117 offset1:1
	ds_write2_b32 v163, v118, v119 offset1:1
	ds_write2_b32 v164, v120, v121 offset1:1
	ds_write2_b32 v165, v122, v123 offset1:1
	ds_write2_b32 v172, v124, v125 offset1:1
	ds_write2_b32 v173, v126, v127 offset1:1
	ds_write2_b32 v174, v128, v129 offset1:1
	s_waitcnt lgkmcnt(0)
	ds_read2_b32 v[70:71], v131 offset1:16
	ds_read2_b32 v[72:73], v131 offset0:65 offset1:81
	ds_read2_b32 v[74:75], v131 offset0:130 offset1:146
	ds_read2_b32 v[78:79], v131 offset0:195 offset1:211
	s_waitcnt lgkmcnt(0)
	v_mul_f32_e32 v67, 0x42800000, v70
	v_mul_f32_e32 v68, 0x42800000, v72
	ds_read2_b32 v[80:81], v136 offset0:4 offset1:20
	ds_read2_b32 v[82:83], v136 offset0:69 offset1:85
	v_cvt_pk_fp8_f32 v66, v67, v68
	v_mul_f32_e32 v69, 0x42800000, v74
	v_mul_f32_e32 v67, 0x42800000, v78
	ds_read2_b32 v[84:85], v136 offset0:134 offset1:150
	ds_read2_b32 v[86:87], v136 offset0:199 offset1:215
	v_cvt_pk_fp8_f32 v66, v69, v67 op_sel:[0,0,1]
	s_waitcnt lgkmcnt(0)
	v_mul_f32_e32 v68, 0x42800000, v80
	v_mul_f32_e32 v69, 0x42800000, v82
	ds_read2_b32 v[88:89], v137 offset0:8 offset1:24
	v_cvt_pk_fp8_f32 v67, v68, v69
	ds_read2_b32 v[90:91], v137 offset0:73 offset1:89
	ds_read2_b32 v[92:93], v137 offset0:138 offset1:154
	ds_read2_b32 v[94:95], v137 offset0:203 offset1:219
	ds_read2_b32 v[96:97], v138 offset0:12 offset1:28
	ds_read2_b32 v[98:99], v138 offset0:77 offset1:93
	s_lshl_b32 s6, s4, 20
	v_mul_f32_e32 v70, 0x42800000, v84
	v_mul_f32_e32 v68, 0x42800000, v86
	s_add_u32 s6, s26, s6
	v_cvt_pk_fp8_f32 v67, v70, v68 op_sel:[0,0,1]
	s_waitcnt lgkmcnt(0)
	v_mul_f32_e32 v69, 0x42800000, v88
	v_mul_f32_e32 v70, 0x42800000, v90
	ds_read2_b32 v[100:101], v138 offset0:142 offset1:158
	ds_read2_b32 v[102:103], v138 offset0:207 offset1:223
	s_addc_u32 s7, s27, 0
	s_lshl_b64 s[4:5], s[4:5], 21
	v_cvt_pk_fp8_f32 v68, v69, v70
	v_mul_f32_e32 v70, 0x42800000, v96
	v_mul_f32_e32 v78, 0x42800000, v98
	s_add_u32 s4, s22, s4
	v_cvt_pk_fp8_f32 v69, v70, v78
	s_addc_u32 s5, s23, s5
	s_cmpk_eq_i32 s29, 0x4000
	v_mul_f32_e32 v72, 0x42800000, v92
	v_mul_f32_e32 v74, 0x42800000, v94
	s_cselect_b32 s4, s6, s4
	v_cvt_pk_fp8_f32 v68, v72, v74 op_sel:[0,0,1]
	s_waitcnt lgkmcnt(0)
	v_mul_f32_e32 v70, 0x42800000, v100
	v_mul_f32_e32 v72, 0x42800000, v102
	s_cselect_b32 s5, s7, s5
	s_add_u32 s4, s4, s28
	v_cvt_pk_fp8_f32 v69, v70, v72 op_sel:[0,0,1]
	v_add_u32_e32 v104, s8, v130
	s_addc_u32 s5, s5, 0
	v_ashrrev_i32_e32 v105, 31, v104
	v_lshl_add_u64 v[76:77], s[4:5], 0, v[166:167]
	v_lshlrev_b64 v[104:105], 10, v[104:105]
	v_lshl_add_u64 v[104:105], v[76:77], 0, v[104:105]
	global_store_dwordx4 v[104:105], v[66:69], off
	v_mul_f32_e32 v70, 0x42800000, v79
	v_mul_f32_e32 v72, 0x42800000, v95
	v_mul_f32_e32 v67, 0x42800000, v71
	v_mul_f32_e32 v68, 0x42800000, v73
	v_cvt_pk_fp8_f32 v66, v67, v68
	v_mul_f32_e32 v68, 0x42800000, v81
	v_mul_f32_e32 v71, 0x42800000, v83
	v_cvt_pk_fp8_f32 v67, v68, v71
	v_mul_f32_e32 v69, 0x42800000, v75
	v_cvt_pk_fp8_f32 v66, v69, v70 op_sel:[0,0,1]
	v_mul_f32_e32 v68, 0x42800000, v85
	v_mul_f32_e32 v69, 0x42800000, v87
	v_cvt_pk_fp8_f32 v67, v68, v69 op_sel:[0,0,1]
	v_mul_f32_e32 v69, 0x42800000, v89
	v_mul_f32_e32 v70, 0x42800000, v91
	v_cvt_pk_fp8_f32 v68, v69, v70
	v_mul_f32_e32 v70, 0x42800000, v97
	v_mul_f32_e32 v73, 0x42800000, v99
	v_cvt_pk_fp8_f32 v69, v70, v73
	v_mul_f32_e32 v71, 0x42800000, v93
	v_cvt_pk_fp8_f32 v68, v71, v72 op_sel:[0,0,1]
	v_mul_f32_e32 v70, 0x42800000, v101
	v_mul_f32_e32 v71, 0x42800000, v103
	v_cvt_pk_fp8_f32 v69, v70, v71 op_sel:[0,0,1]
	v_add_u32_e32 v70, s8, v132
	v_ashrrev_i32_e32 v71, 31, v70
	ds_read2_b32 v[72:73], v131 offset0:32 offset1:48
	ds_read2_b32 v[74:75], v131 offset0:97 offset1:113
	ds_read2_b32 v[78:79], v131 offset0:162 offset1:178
	v_lshlrev_b64 v[70:71], 10, v[70:71]
	v_lshl_add_u64 v[70:71], v[76:77], 0, v[70:71]
	global_store_dwordx4 v[70:71], v[66:69], off
	ds_read2_b32 v[70:71], v131 offset0:227 offset1:243
	ds_read2_b32 v[80:81], v136 offset0:36 offset1:52
	ds_read2_b32 v[82:83], v136 offset0:101 offset1:117
	s_waitcnt lgkmcnt(0)
	v_mul_f32_e32 v67, 0x42800000, v72
	v_mul_f32_e32 v68, 0x42800000, v74
	v_cvt_pk_fp8_f32 v66, v67, v68
	v_mul_f32_e32 v69, 0x42800000, v78
	v_mul_f32_e32 v67, 0x42800000, v70
	ds_read2_b32 v[84:85], v136 offset0:166 offset1:182
	ds_read2_b32 v[86:87], v136 offset0:231 offset1:247
	v_cvt_pk_fp8_f32 v66, v69, v67 op_sel:[0,0,1]
	v_mul_f32_e32 v68, 0x42800000, v80
	v_mul_f32_e32 v69, 0x42800000, v82
	ds_read2_b32 v[88:89], v137 offset0:40 offset1:56
	v_cvt_pk_fp8_f32 v67, v68, v69
	ds_read2_b32 v[90:91], v137 offset0:105 offset1:121
	ds_read2_b32 v[92:93], v137 offset0:170 offset1:186
	ds_read2_b32 v[94:95], v137 offset0:235 offset1:251
	ds_read2_b32 v[96:97], v138 offset0:44 offset1:60
	ds_read2_b32 v[98:99], v138 offset0:109 offset1:125
	s_waitcnt lgkmcnt(0)
	v_mul_f32_e32 v70, 0x42800000, v84
	v_mul_f32_e32 v68, 0x42800000, v86
	v_cvt_pk_fp8_f32 v67, v70, v68 op_sel:[0,0,1]
	v_mul_f32_e32 v69, 0x42800000, v88
	v_mul_f32_e32 v70, 0x42800000, v90
	ds_read2_b32 v[100:101], v138 offset0:174 offset1:190
	ds_read2_b32 v[102:103], v138 offset0:239 offset1:255
	v_cvt_pk_fp8_f32 v68, v69, v70
	v_mul_f32_e32 v70, 0x42800000, v96
	v_mul_f32_e32 v78, 0x42800000, v98
	v_cvt_pk_fp8_f32 v69, v70, v78
	v_mul_f32_e32 v72, 0x42800000, v92
	v_mul_f32_e32 v74, 0x42800000, v94
	v_cvt_pk_fp8_f32 v68, v72, v74 op_sel:[0,0,1]
	s_waitcnt lgkmcnt(0)
	v_mul_f32_e32 v70, 0x42800000, v100
	v_mul_f32_e32 v72, 0x42800000, v102
	v_cvt_pk_fp8_f32 v69, v70, v72 op_sel:[0,0,1]
	v_add_u32_e32 v104, s8, v133
	v_ashrrev_i32_e32 v105, 31, v104
	v_lshlrev_b64 v[104:105], 10, v[104:105]
	v_lshl_add_u64 v[104:105], v[76:77], 0, v[104:105]
	global_store_dwordx4 v[104:105], v[66:69], off
	v_mul_f32_e32 v70, 0x42800000, v71
	v_mul_f32_e32 v71, 0x42800000, v83
	v_mul_f32_e32 v67, 0x42800000, v73
	v_mul_f32_e32 v68, 0x42800000, v75
	v_cvt_pk_fp8_f32 v66, v67, v68
	v_mul_f32_e32 v68, 0x42800000, v81
	v_cvt_pk_fp8_f32 v67, v68, v71
	v_mul_f32_e32 v69, 0x42800000, v79
	v_cvt_pk_fp8_f32 v66, v69, v70 op_sel:[0,0,1]
	v_mul_f32_e32 v68, 0x42800000, v85
	v_mul_f32_e32 v69, 0x42800000, v87
	v_cvt_pk_fp8_f32 v67, v68, v69 op_sel:[0,0,1]
	v_mul_f32_e32 v69, 0x42800000, v89
	v_mul_f32_e32 v70, 0x42800000, v91
	v_cvt_pk_fp8_f32 v68, v69, v70
	v_mul_f32_e32 v70, 0x42800000, v97
	v_mul_f32_e32 v73, 0x42800000, v99
	v_cvt_pk_fp8_f32 v69, v70, v73
	v_mul_f32_e32 v71, 0x42800000, v93
	v_mul_f32_e32 v72, 0x42800000, v95
	v_cvt_pk_fp8_f32 v68, v71, v72 op_sel:[0,0,1]
	v_mul_f32_e32 v70, 0x42800000, v101
	v_mul_f32_e32 v71, 0x42800000, v103
	v_cvt_pk_fp8_f32 v69, v70, v71 op_sel:[0,0,1]
	v_add_u32_e32 v70, s8, v134
	v_ashrrev_i32_e32 v71, 31, v70
	v_lshlrev_b64 v[70:71], 10, v[70:71]
	v_lshl_add_u64 v[70:71], v[76:77], 0, v[70:71]
	global_store_dwordx4 v[70:71], v[66:69], off
	s_waitcnt lgkmcnt(0)
	s_mov_b32 s4, 2
	s_andn2_b64 vcc, exec, s[2:3]
	s_mov_b64 s[10:11], 0
	s_cbranch_vccz .LBB0_915
